# gated-merge GEMM: mid-K gate loads batched; epilogue gate loads 8 in flight with counted waits
# speedup vs baseline: 1.0102x; 1.0102x over previous
;     __device__ __forceinline__ void mid(f32x4 (&acc)[2][2][4][2], const pg8::Unit& u, int wr, int wc, int fr_, int fq) const {
;         int fr = fr_; asm volatile("" : "+v"(fr));
; #pragma unroll
;         for (int ai = 0; ai < 2; ++ai)
; #pragma unroll
;             for (int m = 0; m < 4; ++m)
; #pragma unroll
;                 for (int bj = 0; bj < 2; ++bj) { const size_t o = (size_t)(u.pm * 256 + ai * 128 + wr * 64 + m * 16 + fr) * INCP + u.pn * 256 + bj * 128 + wc * 32 + 8 * fq;
;                     const u32x4 ga = *(const u32x4*)(PROJ + o + C_GA), gb = *(const u32x4*)(PROJ + o + C_GB);
; #pragma unroll
;                     for (int i = 0; i < 4; ++i) { const float r0 = bflo(ga[i]) * __builtin_amdgcn_rcpf(bflo(gb[i])), r1 = bfhi(ga[i]) * __builtin_amdgcn_rcpf(bfhi(gb[i]));
;                         acc[ai][bj][m][i >> 1][2 * (i & 1)] *= r0; acc[ai][bj][m][i >> 1][2 * (i & 1) + 1] *= r1; }
;                     __builtin_amdgcn_sched_barrier(0); }
;     }
.LBB0_1139:
	v_mov_b32_e32 v2, v225
	s_nop 0
	v_add_u32_e32 v2, s42, v2
	v_add_u32_e32 v4, s19, v2
	v_mad_i64_i32 v[4:5], s[26:27], v4, s46, v[212:213]
	v_add_co_u32_e32 v4, vcc, 0x1000, v4
	s_nop 1
	v_addc_co_u32_e32 v5, vcc, 0, v5, vcc
	global_load_dwordx4 v[134:137], v[4:5], off offset:320
	global_load_dwordx4 v[138:141], v[4:5], off offset:2368
	global_load_dwordx4 v[142:145], v[4:5], off offset:576
	global_load_dwordx4 v[146:149], v[4:5], off offset:2624
	v_add_u32_e32 v4, s3, v2
	v_mad_i64_i32 v[4:5], s[26:27], v4, s46, v[212:213]
	v_add_co_u32_e32 v4, vcc, s47, v4
	s_nop 1
	v_addc_co_u32_e32 v5, vcc, 0, v5, vcc
	global_load_dwordx4 v[150:153], v[4:5], off offset:320
	global_load_dwordx4 v[154:157], v[4:5], off offset:2368
	global_load_dwordx4 v[158:161], v[4:5], off offset:576
	global_load_dwordx4 v[162:165], v[4:5], off offset:2624
	v_add_u32_e32 v4, s33, v2
	v_mad_i64_i32 v[4:5], s[26:27], v4, s46, v[212:213]
	v_add_co_u32_e32 v4, vcc, s47, v4
	s_nop 1
	v_addc_co_u32_e32 v5, vcc, 0, v5, vcc
	global_load_dwordx4 v[166:169], v[4:5], off offset:320
	global_load_dwordx4 v[170:173], v[4:5], off offset:2368
	global_load_dwordx4 v[174:177], v[4:5], off offset:576
	global_load_dwordx4 v[178:181], v[4:5], off offset:2624
	v_add_u32_e32 v4, s55, v2
	v_mad_i64_i32 v[4:5], s[26:27], v4, s46, v[212:213]
	v_add_co_u32_e32 v4, vcc, s47, v4
	s_nop 1
	v_addc_co_u32_e32 v5, vcc, 0, v5, vcc
	global_load_dwordx4 v[182:185], v[4:5], off offset:320
	global_load_dwordx4 v[186:189], v[4:5], off offset:2368
	global_load_dwordx4 v[190:193], v[4:5], off offset:576
	global_load_dwordx4 v[194:197], v[4:5], off offset:2624
	s_waitcnt vmcnt(12)
	v_lshlrev_b32_e32 v4, 16, v138
	v_and_b32_e32 v138, 0xffff0000, v138
	v_rcp_f32_e32 v4, v4
	v_rcp_f32_e32 v138, v138
	v_lshlrev_b32_e32 v5, 16, v134
	v_and_b32_e32 v134, 0xffff0000, v134
	v_mul_f32_e32 v4, v4, v5
	v_mul_f32_e32 v134, v138, v134
	v_mul_f32_e32 v130, v130, v4
	v_mul_f32_e32 v131, v131, v134
	v_lshlrev_b32_e32 v4, 16, v139
	v_and_b32_e32 v139, 0xffff0000, v139
	v_rcp_f32_e32 v4, v4
	v_rcp_f32_e32 v139, v139
	v_lshlrev_b32_e32 v5, 16, v135
	v_and_b32_e32 v135, 0xffff0000, v135
	v_mul_f32_e32 v4, v4, v5
	v_mul_f32_e32 v135, v139, v135
	v_mul_f32_e32 v132, v132, v4
	v_mul_f32_e32 v133, v133, v135
	v_lshlrev_b32_e32 v4, 16, v140
	v_and_b32_e32 v140, 0xffff0000, v140
	v_rcp_f32_e32 v4, v4
	v_rcp_f32_e32 v140, v140
	v_lshlrev_b32_e32 v5, 16, v136
	v_and_b32_e32 v136, 0xffff0000, v136
	v_mul_f32_e32 v4, v4, v5
	v_mul_f32_e32 v136, v140, v136
	v_mul_f32_e32 v126, v126, v4
	v_mul_f32_e32 v127, v127, v136
	v_lshlrev_b32_e32 v4, 16, v141
	v_and_b32_e32 v141, 0xffff0000, v141
	v_rcp_f32_e32 v4, v4
	v_rcp_f32_e32 v141, v141
	v_lshlrev_b32_e32 v5, 16, v137
	v_and_b32_e32 v137, 0xffff0000, v137
	v_mul_f32_e32 v4, v4, v5
	v_mul_f32_e32 v137, v141, v137
	v_mul_f32_e32 v128, v128, v4
	v_mul_f32_e32 v129, v129, v137
	v_lshlrev_b32_e32 v4, 16, v146
	v_and_b32_e32 v146, 0xffff0000, v146
	v_rcp_f32_e32 v4, v4
	v_rcp_f32_e32 v146, v146
	v_lshlrev_b32_e32 v5, 16, v142
	v_and_b32_e32 v142, 0xffff0000, v142
	v_mul_f32_e32 v4, v4, v5
	v_mul_f32_e32 v142, v146, v142
	v_mul_f32_e32 v122, v122, v4
	v_mul_f32_e32 v123, v123, v142
	v_lshlrev_b32_e32 v4, 16, v147
	v_and_b32_e32 v147, 0xffff0000, v147
	v_rcp_f32_e32 v4, v4
	v_rcp_f32_e32 v147, v147
	v_lshlrev_b32_e32 v5, 16, v143
	v_and_b32_e32 v143, 0xffff0000, v143
	v_mul_f32_e32 v4, v4, v5
	v_mul_f32_e32 v143, v147, v143
	v_mul_f32_e32 v124, v124, v4
	v_mul_f32_e32 v125, v125, v143
	v_lshlrev_b32_e32 v4, 16, v148
	v_and_b32_e32 v148, 0xffff0000, v148
	v_rcp_f32_e32 v4, v4
	v_rcp_f32_e32 v148, v148
	v_lshlrev_b32_e32 v5, 16, v144
	v_and_b32_e32 v144, 0xffff0000, v144
	v_mul_f32_e32 v4, v4, v5
	v_mul_f32_e32 v144, v148, v144
	v_mul_f32_e32 v118, v118, v4
	v_mul_f32_e32 v119, v119, v144
	v_lshlrev_b32_e32 v4, 16, v149
	v_and_b32_e32 v149, 0xffff0000, v149
	v_rcp_f32_e32 v4, v4
	v_rcp_f32_e32 v149, v149
	v_lshlrev_b32_e32 v5, 16, v145
	v_and_b32_e32 v145, 0xffff0000, v145
	v_mul_f32_e32 v4, v4, v5
	v_mul_f32_e32 v145, v149, v145
	v_mul_f32_e32 v120, v120, v4
	v_mul_f32_e32 v121, v121, v145
	s_waitcnt vmcnt(8)
	v_lshlrev_b32_e32 v4, 16, v154
	v_and_b32_e32 v154, 0xffff0000, v154
	v_rcp_f32_e32 v4, v4
	v_rcp_f32_e32 v154, v154
	v_lshlrev_b32_e32 v5, 16, v150
	v_and_b32_e32 v150, 0xffff0000, v150
	v_mul_f32_e32 v4, v4, v5
	v_mul_f32_e32 v150, v154, v150
	v_mul_f32_e32 v114, v114, v4
	v_mul_f32_e32 v115, v115, v150
	v_lshlrev_b32_e32 v4, 16, v155
	v_and_b32_e32 v155, 0xffff0000, v155
	v_rcp_f32_e32 v4, v4
	v_rcp_f32_e32 v155, v155
	v_lshlrev_b32_e32 v5, 16, v151
	v_and_b32_e32 v151, 0xffff0000, v151
	v_mul_f32_e32 v4, v4, v5
	v_mul_f32_e32 v151, v155, v151
	v_mul_f32_e32 v116, v116, v4
	v_mul_f32_e32 v117, v117, v151
	v_lshlrev_b32_e32 v4, 16, v156
	v_and_b32_e32 v156, 0xffff0000, v156
	v_rcp_f32_e32 v4, v4
	v_rcp_f32_e32 v156, v156
	v_lshlrev_b32_e32 v5, 16, v152
	v_and_b32_e32 v152, 0xffff0000, v152
	v_mul_f32_e32 v4, v4, v5
	v_mul_f32_e32 v152, v156, v152
	v_mul_f32_e32 v110, v110, v4
	v_mul_f32_e32 v111, v111, v152
	v_lshlrev_b32_e32 v4, 16, v157
	v_and_b32_e32 v157, 0xffff0000, v157
	v_rcp_f32_e32 v4, v4
	v_rcp_f32_e32 v157, v157
	v_lshlrev_b32_e32 v5, 16, v153
	v_and_b32_e32 v153, 0xffff0000, v153
	v_mul_f32_e32 v4, v4, v5
	v_mul_f32_e32 v153, v157, v153
	v_mul_f32_e32 v112, v112, v4
	v_mul_f32_e32 v113, v113, v153
	v_lshlrev_b32_e32 v4, 16, v162
	v_and_b32_e32 v162, 0xffff0000, v162
	v_rcp_f32_e32 v4, v4
	v_rcp_f32_e32 v162, v162
	v_lshlrev_b32_e32 v5, 16, v158
	v_and_b32_e32 v158, 0xffff0000, v158
	v_mul_f32_e32 v4, v4, v5
	v_mul_f32_e32 v158, v162, v158
	v_mul_f32_e32 v106, v106, v4
	v_mul_f32_e32 v107, v107, v158
	v_lshlrev_b32_e32 v4, 16, v163
	v_and_b32_e32 v163, 0xffff0000, v163
	v_rcp_f32_e32 v4, v4
	v_rcp_f32_e32 v163, v163
	v_lshlrev_b32_e32 v5, 16, v159
	v_and_b32_e32 v159, 0xffff0000, v159
	v_mul_f32_e32 v4, v4, v5
	v_mul_f32_e32 v159, v163, v159
	v_mul_f32_e32 v108, v108, v4
	v_mul_f32_e32 v109, v109, v159
	v_lshlrev_b32_e32 v4, 16, v164
	v_and_b32_e32 v164, 0xffff0000, v164
	v_rcp_f32_e32 v4, v4
	v_rcp_f32_e32 v164, v164
	v_lshlrev_b32_e32 v5, 16, v160
	v_and_b32_e32 v160, 0xffff0000, v160
	v_mul_f32_e32 v4, v4, v5
	v_mul_f32_e32 v160, v164, v160
	v_mul_f32_e32 v102, v102, v4
	v_mul_f32_e32 v103, v103, v160
	v_lshlrev_b32_e32 v4, 16, v165
	v_and_b32_e32 v165, 0xffff0000, v165
	v_rcp_f32_e32 v4, v4
	v_rcp_f32_e32 v165, v165
	v_lshlrev_b32_e32 v5, 16, v161
	v_and_b32_e32 v161, 0xffff0000, v161
	v_mul_f32_e32 v4, v4, v5
	v_mul_f32_e32 v161, v165, v161
	v_mul_f32_e32 v104, v104, v4
	v_mul_f32_e32 v105, v105, v161
	s_waitcnt vmcnt(4)
;     __device__ __forceinline__ void mid(f32x4 (&acc)[2][2][4][2], const pg8::Unit& u, int wr, int wc, int fr_, int fq) const {
;         int fr = fr_; asm volatile("" : "+v"(fr));
; #pragma unroll
;         for (int ai = 0; ai < 2; ++ai)
; #pragma unroll
;             for (int m = 0; m < 4; ++m)
; #pragma unroll
;                 for (int bj = 0; bj < 2; ++bj) { const size_t o = (size_t)(u.pm * 256 + ai * 128 + wr * 64 + m * 16 + fr) * INCP + u.pn * 256 + bj * 128 + wc * 32 + 8 * fq;
;                     const u32x4 ga = *(const u32x4*)(PROJ + o + C_GA), gb = *(const u32x4*)(PROJ + o + C_GB);
; #pragma unroll
;                     for (int i = 0; i < 4; ++i) { const float r0 = bflo(ga[i]) * __builtin_amdgcn_rcpf(bflo(gb[i])), r1 = bfhi(ga[i]) * __builtin_amdgcn_rcpf(bfhi(gb[i]));
;                         acc[ai][bj][m][i >> 1][2 * (i & 1)] *= r0; acc[ai][bj][m][i >> 1][2 * (i & 1) + 1] *= r1; }
;                     __builtin_amdgcn_sched_barrier(0); }
;     }
	v_lshlrev_b32_e32 v4, 16, v170
	v_and_b32_e32 v170, 0xffff0000, v170
	v_rcp_f32_e32 v4, v4
	v_rcp_f32_e32 v170, v170
	v_lshlrev_b32_e32 v5, 16, v166
	v_and_b32_e32 v166, 0xffff0000, v166
	v_mul_f32_e32 v4, v4, v5
	v_mul_f32_e32 v166, v170, v166
	v_mul_f32_e32 v98, v98, v4
	v_mul_f32_e32 v99, v99, v166
	v_lshlrev_b32_e32 v4, 16, v171
	v_and_b32_e32 v171, 0xffff0000, v171
	v_rcp_f32_e32 v4, v4
	v_rcp_f32_e32 v171, v171
	v_lshlrev_b32_e32 v5, 16, v167
	v_and_b32_e32 v167, 0xffff0000, v167
	v_mul_f32_e32 v4, v4, v5
	v_mul_f32_e32 v167, v171, v167
	v_mul_f32_e32 v100, v100, v4
	v_mul_f32_e32 v101, v101, v167
	v_lshlrev_b32_e32 v4, 16, v172
	v_and_b32_e32 v172, 0xffff0000, v172
	v_rcp_f32_e32 v4, v4
	v_rcp_f32_e32 v172, v172
	v_lshlrev_b32_e32 v5, 16, v168
	v_and_b32_e32 v168, 0xffff0000, v168
	v_mul_f32_e32 v4, v4, v5
	v_mul_f32_e32 v168, v172, v168
	v_mul_f32_e32 v94, v94, v4
	v_mul_f32_e32 v95, v95, v168
	v_lshlrev_b32_e32 v4, 16, v173
	v_and_b32_e32 v173, 0xffff0000, v173
	v_rcp_f32_e32 v4, v4
	v_rcp_f32_e32 v173, v173
	v_lshlrev_b32_e32 v5, 16, v169
	v_and_b32_e32 v169, 0xffff0000, v169
	v_mul_f32_e32 v4, v4, v5
	v_mul_f32_e32 v169, v173, v169
	v_mul_f32_e32 v96, v96, v4
	v_mul_f32_e32 v97, v97, v169
	v_lshlrev_b32_e32 v4, 16, v178
	v_and_b32_e32 v178, 0xffff0000, v178
	v_rcp_f32_e32 v4, v4
	v_rcp_f32_e32 v178, v178
	v_lshlrev_b32_e32 v5, 16, v174
	v_and_b32_e32 v174, 0xffff0000, v174
	v_mul_f32_e32 v4, v4, v5
	v_mul_f32_e32 v174, v178, v174
	v_mul_f32_e32 v90, v90, v4
	v_mul_f32_e32 v91, v91, v174
	v_lshlrev_b32_e32 v4, 16, v179
	v_and_b32_e32 v179, 0xffff0000, v179
	v_rcp_f32_e32 v4, v4
	v_rcp_f32_e32 v179, v179
	v_lshlrev_b32_e32 v5, 16, v175
	v_and_b32_e32 v175, 0xffff0000, v175
	v_mul_f32_e32 v4, v4, v5
	v_mul_f32_e32 v175, v179, v175
	v_mul_f32_e32 v92, v92, v4
	v_mul_f32_e32 v93, v93, v175
	v_lshlrev_b32_e32 v4, 16, v180
	v_and_b32_e32 v180, 0xffff0000, v180
	v_rcp_f32_e32 v4, v4
	v_rcp_f32_e32 v180, v180
	v_lshlrev_b32_e32 v5, 16, v176
	v_and_b32_e32 v176, 0xffff0000, v176
	v_mul_f32_e32 v4, v4, v5
	v_mul_f32_e32 v176, v180, v176
	v_mul_f32_e32 v86, v86, v4
	v_mul_f32_e32 v87, v87, v176
	v_lshlrev_b32_e32 v4, 16, v181
	v_and_b32_e32 v181, 0xffff0000, v181
	v_rcp_f32_e32 v4, v4
	v_rcp_f32_e32 v181, v181
	v_lshlrev_b32_e32 v5, 16, v177
	v_and_b32_e32 v177, 0xffff0000, v177
	v_mul_f32_e32 v4, v4, v5
	v_mul_f32_e32 v177, v181, v177
	v_mul_f32_e32 v88, v88, v4
	v_mul_f32_e32 v89, v89, v177
	s_waitcnt vmcnt(0)
	v_lshlrev_b32_e32 v4, 16, v186
	v_and_b32_e32 v186, 0xffff0000, v186
	v_rcp_f32_e32 v4, v4
	v_rcp_f32_e32 v186, v186
	v_lshlrev_b32_e32 v5, 16, v182
	v_and_b32_e32 v182, 0xffff0000, v182
	v_mul_f32_e32 v4, v4, v5
	v_mul_f32_e32 v182, v186, v182
	v_mul_f32_e32 v82, v82, v4
	v_mul_f32_e32 v83, v83, v182
	v_lshlrev_b32_e32 v4, 16, v187
	v_and_b32_e32 v187, 0xffff0000, v187
	v_rcp_f32_e32 v4, v4
	v_rcp_f32_e32 v187, v187
	v_lshlrev_b32_e32 v5, 16, v183
	v_and_b32_e32 v183, 0xffff0000, v183
	v_mul_f32_e32 v4, v4, v5
	v_mul_f32_e32 v183, v187, v183
	v_mul_f32_e32 v84, v84, v4
	v_mul_f32_e32 v85, v85, v183
	v_lshlrev_b32_e32 v4, 16, v188
	v_and_b32_e32 v188, 0xffff0000, v188
	v_rcp_f32_e32 v4, v4
	v_rcp_f32_e32 v188, v188
	v_lshlrev_b32_e32 v5, 16, v184
	v_and_b32_e32 v184, 0xffff0000, v184
	v_mul_f32_e32 v4, v4, v5
	v_mul_f32_e32 v184, v188, v184
	v_mul_f32_e32 v78, v78, v4
	v_mul_f32_e32 v79, v79, v184
	v_lshlrev_b32_e32 v4, 16, v189
	v_and_b32_e32 v189, 0xffff0000, v189
	v_rcp_f32_e32 v4, v4
	v_rcp_f32_e32 v189, v189
	v_lshlrev_b32_e32 v5, 16, v185
	v_and_b32_e32 v185, 0xffff0000, v185
	v_mul_f32_e32 v4, v4, v5
	v_mul_f32_e32 v185, v189, v185
	v_mul_f32_e32 v80, v80, v4
	v_mul_f32_e32 v81, v81, v185
	v_lshlrev_b32_e32 v4, 16, v194
	v_and_b32_e32 v194, 0xffff0000, v194
	v_rcp_f32_e32 v4, v4
	v_rcp_f32_e32 v194, v194
	v_lshlrev_b32_e32 v5, 16, v190
	v_and_b32_e32 v190, 0xffff0000, v190
	v_mul_f32_e32 v4, v4, v5
	v_mul_f32_e32 v190, v194, v190
	v_mul_f32_e32 v74, v74, v4
	v_mul_f32_e32 v75, v75, v190
	v_lshlrev_b32_e32 v4, 16, v195
	v_and_b32_e32 v195, 0xffff0000, v195
	v_rcp_f32_e32 v4, v4
	v_rcp_f32_e32 v195, v195
	v_lshlrev_b32_e32 v5, 16, v191
	v_and_b32_e32 v191, 0xffff0000, v191
	v_mul_f32_e32 v4, v4, v5
	v_mul_f32_e32 v191, v195, v191
	v_mul_f32_e32 v76, v76, v4
	v_mul_f32_e32 v77, v77, v191
	v_lshlrev_b32_e32 v4, 16, v196
	v_and_b32_e32 v196, 0xffff0000, v196
	v_rcp_f32_e32 v4, v4
	v_rcp_f32_e32 v196, v196
	v_lshlrev_b32_e32 v5, 16, v192
	v_and_b32_e32 v192, 0xffff0000, v192
	v_mul_f32_e32 v4, v4, v5
	v_mul_f32_e32 v192, v196, v192
	v_mul_f32_e32 v70, v70, v4
	v_mul_f32_e32 v71, v71, v192
	v_lshlrev_b32_e32 v4, 16, v197
	v_and_b32_e32 v197, 0xffff0000, v197
	v_rcp_f32_e32 v4, v4
	v_rcp_f32_e32 v197, v197
	v_lshlrev_b32_e32 v5, 16, v193
	v_and_b32_e32 v193, 0xffff0000, v193
	v_mul_f32_e32 v4, v4, v5
	v_mul_f32_e32 v193, v197, v193
	v_mul_f32_e32 v72, v72, v4
	v_mul_f32_e32 v73, v73, v193
	v_add_u32_e32 v4, s56, v2
	v_mad_i64_i32 v[4:5], s[26:27], v4, s46, v[212:213]
	v_add_co_u32_e32 v4, vcc, s47, v4
	s_nop 1
	v_addc_co_u32_e32 v5, vcc, 0, v5, vcc
	global_load_dwordx4 v[134:137], v[4:5], off offset:320
	global_load_dwordx4 v[138:141], v[4:5], off offset:2368
	global_load_dwordx4 v[142:145], v[4:5], off offset:576
	global_load_dwordx4 v[146:149], v[4:5], off offset:2624
	v_add_u32_e32 v4, s57, v2
	v_mad_i64_i32 v[4:5], s[26:27], v4, s46, v[212:213]
	v_add_co_u32_e32 v4, vcc, s47, v4
	s_nop 1
	v_addc_co_u32_e32 v5, vcc, 0, v5, vcc
	global_load_dwordx4 v[150:153], v[4:5], off offset:320
	global_load_dwordx4 v[154:157], v[4:5], off offset:2368
	global_load_dwordx4 v[158:161], v[4:5], off offset:576
	global_load_dwordx4 v[162:165], v[4:5], off offset:2624
	v_add_u32_e32 v4, s58, v2
	v_mad_i64_i32 v[4:5], s[26:27], v4, s46, v[212:213]
	v_add_co_u32_e32 v4, vcc, s47, v4
	s_nop 1
	v_addc_co_u32_e32 v5, vcc, 0, v5, vcc
	global_load_dwordx4 v[166:169], v[4:5], off offset:320
	global_load_dwordx4 v[170:173], v[4:5], off offset:2368
	global_load_dwordx4 v[174:177], v[4:5], off offset:576
	global_load_dwordx4 v[178:181], v[4:5], off offset:2624
	v_add_u32_e32 v2, s59, v2
	v_mad_i64_i32 v[4:5], s[26:27], v2, s46, v[212:213]
	v_add_co_u32_e32 v4, vcc, s47, v4
	s_nop 1
	v_addc_co_u32_e32 v5, vcc, 0, v5, vcc
	global_load_dwordx4 v[182:185], v[4:5], off offset:320
	global_load_dwordx4 v[186:189], v[4:5], off offset:2368
	global_load_dwordx4 v[190:193], v[4:5], off offset:576
	global_load_dwordx4 v[194:197], v[4:5], off offset:2624
	s_waitcnt vmcnt(12)
;     __device__ __forceinline__ void mid(f32x4 (&acc)[2][2][4][2], const pg8::Unit& u, int wr, int wc, int fr_, int fq) const {
;         int fr = fr_; asm volatile("" : "+v"(fr));
; #pragma unroll
;         for (int ai = 0; ai < 2; ++ai)
; #pragma unroll
;             for (int m = 0; m < 4; ++m)
; #pragma unroll
;                 for (int bj = 0; bj < 2; ++bj) { const size_t o = (size_t)(u.pm * 256 + ai * 128 + wr * 64 + m * 16 + fr) * INCP + u.pn * 256 + bj * 128 + wc * 32 + 8 * fq;
;                     const u32x4 ga = *(const u32x4*)(PROJ + o + C_GA), gb = *(const u32x4*)(PROJ + o + C_GB);
; #pragma unroll
;                     for (int i = 0; i < 4; ++i) { const float r0 = bflo(ga[i]) * __builtin_amdgcn_rcpf(bflo(gb[i])), r1 = bfhi(ga[i]) * __builtin_amdgcn_rcpf(bfhi(gb[i]));
;                         acc[ai][bj][m][i >> 1][2 * (i & 1)] *= r0; acc[ai][bj][m][i >> 1][2 * (i & 1) + 1] *= r1; }
;                     __builtin_amdgcn_sched_barrier(0); }
;     }
	v_lshlrev_b32_e32 v4, 16, v138
	v_and_b32_e32 v138, 0xffff0000, v138
	v_rcp_f32_e32 v4, v4
	v_rcp_f32_e32 v138, v138
	v_lshlrev_b32_e32 v5, 16, v134
	v_and_b32_e32 v134, 0xffff0000, v134
	v_mul_f32_e32 v4, v4, v5
	v_mul_f32_e32 v134, v138, v134
	v_mul_f32_e32 v66, v66, v4
	v_mul_f32_e32 v67, v67, v134
	v_lshlrev_b32_e32 v4, 16, v139
	v_and_b32_e32 v139, 0xffff0000, v139
	v_rcp_f32_e32 v4, v4
	v_rcp_f32_e32 v139, v139
	v_lshlrev_b32_e32 v5, 16, v135
	v_and_b32_e32 v135, 0xffff0000, v135
	v_mul_f32_e32 v4, v4, v5
	v_mul_f32_e32 v135, v139, v135
	v_mul_f32_e32 v68, v68, v4
	v_mul_f32_e32 v69, v69, v135
	v_lshlrev_b32_e32 v4, 16, v140
	v_and_b32_e32 v140, 0xffff0000, v140
	v_rcp_f32_e32 v4, v4
	v_rcp_f32_e32 v140, v140
	v_lshlrev_b32_e32 v5, 16, v136
	v_and_b32_e32 v136, 0xffff0000, v136
	v_mul_f32_e32 v4, v4, v5
	v_mul_f32_e32 v136, v140, v136
	v_mul_f32_e32 v62, v62, v4
	v_mul_f32_e32 v63, v63, v136
	v_lshlrev_b32_e32 v4, 16, v141
	v_and_b32_e32 v141, 0xffff0000, v141
	v_rcp_f32_e32 v4, v4
	v_rcp_f32_e32 v141, v141
	v_lshlrev_b32_e32 v5, 16, v137
	v_and_b32_e32 v137, 0xffff0000, v137
	v_mul_f32_e32 v4, v4, v5
	v_mul_f32_e32 v137, v141, v137
	v_mul_f32_e32 v64, v64, v4
	v_mul_f32_e32 v65, v65, v137
	v_lshlrev_b32_e32 v4, 16, v146
	v_and_b32_e32 v146, 0xffff0000, v146
	v_rcp_f32_e32 v4, v4
	v_rcp_f32_e32 v146, v146
	v_lshlrev_b32_e32 v5, 16, v142
	v_and_b32_e32 v142, 0xffff0000, v142
	v_mul_f32_e32 v4, v4, v5
	v_mul_f32_e32 v142, v146, v142
	v_mul_f32_e32 v58, v58, v4
	v_mul_f32_e32 v59, v59, v142
	v_lshlrev_b32_e32 v4, 16, v147
	v_and_b32_e32 v147, 0xffff0000, v147
	v_rcp_f32_e32 v4, v4
	v_rcp_f32_e32 v147, v147
	v_lshlrev_b32_e32 v5, 16, v143
	v_and_b32_e32 v143, 0xffff0000, v143
	v_mul_f32_e32 v4, v4, v5
	v_mul_f32_e32 v143, v147, v143
	v_mul_f32_e32 v60, v60, v4
	v_mul_f32_e32 v61, v61, v143
	v_lshlrev_b32_e32 v4, 16, v148
	v_and_b32_e32 v148, 0xffff0000, v148
	v_rcp_f32_e32 v4, v4
	v_rcp_f32_e32 v148, v148
	v_lshlrev_b32_e32 v5, 16, v144
	v_and_b32_e32 v144, 0xffff0000, v144
	v_mul_f32_e32 v4, v4, v5
	v_mul_f32_e32 v144, v148, v144
	v_mul_f32_e32 v54, v54, v4
	v_mul_f32_e32 v55, v55, v144
	v_lshlrev_b32_e32 v4, 16, v149
	v_and_b32_e32 v149, 0xffff0000, v149
	v_rcp_f32_e32 v4, v4
	v_rcp_f32_e32 v149, v149
	v_lshlrev_b32_e32 v5, 16, v145
	v_and_b32_e32 v145, 0xffff0000, v145
	v_mul_f32_e32 v4, v4, v5
	v_mul_f32_e32 v145, v149, v145
	v_mul_f32_e32 v56, v56, v4
	v_mul_f32_e32 v57, v57, v145
	s_waitcnt vmcnt(8)
	v_lshlrev_b32_e32 v4, 16, v154
	v_and_b32_e32 v154, 0xffff0000, v154
	v_rcp_f32_e32 v4, v4
	v_rcp_f32_e32 v154, v154
	v_lshlrev_b32_e32 v5, 16, v150
	v_and_b32_e32 v150, 0xffff0000, v150
	v_mul_f32_e32 v4, v4, v5
	v_mul_f32_e32 v150, v154, v150
	v_mul_f32_e32 v50, v50, v4
	v_mul_f32_e32 v51, v51, v150
	v_lshlrev_b32_e32 v4, 16, v155
	v_and_b32_e32 v155, 0xffff0000, v155
	v_rcp_f32_e32 v4, v4
	v_rcp_f32_e32 v155, v155
	v_lshlrev_b32_e32 v5, 16, v151
	v_and_b32_e32 v151, 0xffff0000, v151
	v_mul_f32_e32 v4, v4, v5
	v_mul_f32_e32 v151, v155, v151
	v_mul_f32_e32 v52, v52, v4
	v_mul_f32_e32 v53, v53, v151
	v_lshlrev_b32_e32 v4, 16, v156
	v_and_b32_e32 v156, 0xffff0000, v156
	v_rcp_f32_e32 v4, v4
	v_rcp_f32_e32 v156, v156
	v_lshlrev_b32_e32 v5, 16, v152
	v_and_b32_e32 v152, 0xffff0000, v152
	v_mul_f32_e32 v4, v4, v5
	v_mul_f32_e32 v152, v156, v152
	v_mul_f32_e32 v46, v46, v4
	v_mul_f32_e32 v47, v47, v152
	v_lshlrev_b32_e32 v4, 16, v157
	v_and_b32_e32 v157, 0xffff0000, v157
	v_rcp_f32_e32 v4, v4
	v_rcp_f32_e32 v157, v157
	v_lshlrev_b32_e32 v5, 16, v153
	v_and_b32_e32 v153, 0xffff0000, v153
	v_mul_f32_e32 v4, v4, v5
	v_mul_f32_e32 v153, v157, v153
	v_mul_f32_e32 v48, v48, v4
	v_mul_f32_e32 v49, v49, v153
	v_lshlrev_b32_e32 v4, 16, v162
	v_and_b32_e32 v162, 0xffff0000, v162
	v_rcp_f32_e32 v4, v4
	v_rcp_f32_e32 v162, v162
	v_lshlrev_b32_e32 v5, 16, v158
	v_and_b32_e32 v158, 0xffff0000, v158
	v_mul_f32_e32 v4, v4, v5
	v_mul_f32_e32 v158, v162, v158
	v_mul_f32_e32 v42, v42, v4
	v_mul_f32_e32 v43, v43, v158
	v_lshlrev_b32_e32 v4, 16, v163
	v_and_b32_e32 v163, 0xffff0000, v163
	v_rcp_f32_e32 v4, v4
	v_rcp_f32_e32 v163, v163
	v_lshlrev_b32_e32 v5, 16, v159
	v_and_b32_e32 v159, 0xffff0000, v159
	v_mul_f32_e32 v4, v4, v5
	v_mul_f32_e32 v159, v163, v159
	v_mul_f32_e32 v44, v44, v4
	v_mul_f32_e32 v45, v45, v159
	v_lshlrev_b32_e32 v4, 16, v164
	v_and_b32_e32 v164, 0xffff0000, v164
	v_rcp_f32_e32 v4, v4
	v_rcp_f32_e32 v164, v164
	v_lshlrev_b32_e32 v5, 16, v160
	v_and_b32_e32 v160, 0xffff0000, v160
	v_mul_f32_e32 v4, v4, v5
	v_mul_f32_e32 v160, v164, v160
	v_mul_f32_e32 v38, v38, v4
	v_mul_f32_e32 v39, v39, v160
	v_lshlrev_b32_e32 v4, 16, v165
	v_and_b32_e32 v165, 0xffff0000, v165
	v_rcp_f32_e32 v4, v4
	v_rcp_f32_e32 v165, v165
	v_lshlrev_b32_e32 v5, 16, v161
	v_and_b32_e32 v161, 0xffff0000, v161
	v_mul_f32_e32 v4, v4, v5
	v_mul_f32_e32 v161, v165, v161
	v_mul_f32_e32 v40, v40, v4
	v_mul_f32_e32 v41, v41, v161
	s_waitcnt vmcnt(4)
;     __device__ __forceinline__ void mid(f32x4 (&acc)[2][2][4][2], const pg8::Unit& u, int wr, int wc, int fr_, int fq) const {
;         int fr = fr_; asm volatile("" : "+v"(fr));
; #pragma unroll
;         for (int ai = 0; ai < 2; ++ai)
; #pragma unroll
;             for (int m = 0; m < 4; ++m)
; #pragma unroll
;                 for (int bj = 0; bj < 2; ++bj) { const size_t o = (size_t)(u.pm * 256 + ai * 128 + wr * 64 + m * 16 + fr) * INCP + u.pn * 256 + bj * 128 + wc * 32 + 8 * fq;
;                     const u32x4 ga = *(const u32x4*)(PROJ + o + C_GA), gb = *(const u32x4*)(PROJ + o + C_GB);
; #pragma unroll
;                     for (int i = 0; i < 4; ++i) { const float r0 = bflo(ga[i]) * __builtin_amdgcn_rcpf(bflo(gb[i])), r1 = bfhi(ga[i]) * __builtin_amdgcn_rcpf(bfhi(gb[i]));
;                         acc[ai][bj][m][i >> 1][2 * (i & 1)] *= r0; acc[ai][bj][m][i >> 1][2 * (i & 1) + 1] *= r1; }
;                     __builtin_amdgcn_sched_barrier(0); }
;     }
	v_lshlrev_b32_e32 v4, 16, v170
	v_and_b32_e32 v170, 0xffff0000, v170
	v_rcp_f32_e32 v4, v4
	v_rcp_f32_e32 v170, v170
	v_lshlrev_b32_e32 v5, 16, v166
	v_and_b32_e32 v166, 0xffff0000, v166
	v_mul_f32_e32 v4, v4, v5
	v_mul_f32_e32 v166, v170, v166
	v_mul_f32_e32 v34, v34, v4
	v_mul_f32_e32 v35, v35, v166
	v_lshlrev_b32_e32 v4, 16, v171
	v_and_b32_e32 v171, 0xffff0000, v171
	v_rcp_f32_e32 v4, v4
	v_rcp_f32_e32 v171, v171
	v_lshlrev_b32_e32 v5, 16, v167
	v_and_b32_e32 v167, 0xffff0000, v167
	v_mul_f32_e32 v4, v4, v5
	v_mul_f32_e32 v167, v171, v167
	v_mul_f32_e32 v36, v36, v4
	v_mul_f32_e32 v37, v37, v167
	v_lshlrev_b32_e32 v4, 16, v172
	v_and_b32_e32 v172, 0xffff0000, v172
	v_rcp_f32_e32 v4, v4
	v_rcp_f32_e32 v172, v172
	v_lshlrev_b32_e32 v5, 16, v168
	v_and_b32_e32 v168, 0xffff0000, v168
	v_mul_f32_e32 v4, v4, v5
	v_mul_f32_e32 v168, v172, v168
	v_mul_f32_e32 v30, v30, v4
	v_mul_f32_e32 v31, v31, v168
	v_lshlrev_b32_e32 v4, 16, v173
	v_and_b32_e32 v173, 0xffff0000, v173
	v_rcp_f32_e32 v4, v4
	v_rcp_f32_e32 v173, v173
	v_lshlrev_b32_e32 v5, 16, v169
	v_and_b32_e32 v169, 0xffff0000, v169
	v_mul_f32_e32 v4, v4, v5
	v_mul_f32_e32 v169, v173, v169
	v_mul_f32_e32 v32, v32, v4
	v_mul_f32_e32 v33, v33, v169
	v_lshlrev_b32_e32 v4, 16, v178
	v_and_b32_e32 v178, 0xffff0000, v178
	v_rcp_f32_e32 v4, v4
	v_rcp_f32_e32 v178, v178
	v_lshlrev_b32_e32 v5, 16, v174
	v_and_b32_e32 v174, 0xffff0000, v174
	v_mul_f32_e32 v4, v4, v5
	v_mul_f32_e32 v174, v178, v174
	v_mul_f32_e32 v26, v26, v4
	v_mul_f32_e32 v27, v27, v174
	v_lshlrev_b32_e32 v4, 16, v179
	v_and_b32_e32 v179, 0xffff0000, v179
	v_rcp_f32_e32 v4, v4
	v_rcp_f32_e32 v179, v179
	v_lshlrev_b32_e32 v5, 16, v175
	v_and_b32_e32 v175, 0xffff0000, v175
	v_mul_f32_e32 v4, v4, v5
	v_mul_f32_e32 v175, v179, v175
	v_mul_f32_e32 v28, v28, v4
	v_mul_f32_e32 v29, v29, v175
	v_lshlrev_b32_e32 v4, 16, v180
	v_and_b32_e32 v180, 0xffff0000, v180
	v_rcp_f32_e32 v4, v4
	v_rcp_f32_e32 v180, v180
	v_lshlrev_b32_e32 v5, 16, v176
	v_and_b32_e32 v176, 0xffff0000, v176
	v_mul_f32_e32 v4, v4, v5
	v_mul_f32_e32 v176, v180, v176
	v_mul_f32_e32 v22, v22, v4
	v_mul_f32_e32 v23, v23, v176
	v_lshlrev_b32_e32 v4, 16, v181
	v_and_b32_e32 v181, 0xffff0000, v181
	v_rcp_f32_e32 v4, v4
	v_rcp_f32_e32 v181, v181
	v_lshlrev_b32_e32 v5, 16, v177
	v_and_b32_e32 v177, 0xffff0000, v177
	v_mul_f32_e32 v4, v4, v5
	v_mul_f32_e32 v177, v181, v177
	v_mul_f32_e32 v24, v24, v4
	v_mul_f32_e32 v25, v25, v177
	s_waitcnt vmcnt(0)
	v_lshlrev_b32_e32 v4, 16, v186
	v_and_b32_e32 v186, 0xffff0000, v186
	v_rcp_f32_e32 v4, v4
	v_rcp_f32_e32 v186, v186
	v_lshlrev_b32_e32 v5, 16, v182
	v_and_b32_e32 v182, 0xffff0000, v182
	v_mul_f32_e32 v4, v4, v5
	v_mul_f32_e32 v182, v186, v182
	v_mul_f32_e32 v18, v18, v4
	v_mul_f32_e32 v19, v19, v182
	v_lshlrev_b32_e32 v4, 16, v187
	v_and_b32_e32 v187, 0xffff0000, v187
	v_rcp_f32_e32 v4, v4
	v_rcp_f32_e32 v187, v187
	v_lshlrev_b32_e32 v5, 16, v183
	v_and_b32_e32 v183, 0xffff0000, v183
	v_mul_f32_e32 v4, v4, v5
	v_mul_f32_e32 v183, v187, v183
	v_mul_f32_e32 v20, v20, v4
	v_mul_f32_e32 v21, v21, v183
	v_lshlrev_b32_e32 v4, 16, v188
	v_and_b32_e32 v188, 0xffff0000, v188
	v_rcp_f32_e32 v4, v4
	v_rcp_f32_e32 v188, v188
	v_lshlrev_b32_e32 v5, 16, v184
	v_and_b32_e32 v184, 0xffff0000, v184
	v_mul_f32_e32 v4, v4, v5
	v_mul_f32_e32 v184, v188, v184
	v_mul_f32_e32 v14, v14, v4
	v_mul_f32_e32 v15, v15, v184
	v_lshlrev_b32_e32 v4, 16, v189
	v_and_b32_e32 v189, 0xffff0000, v189
	v_rcp_f32_e32 v4, v4
	v_rcp_f32_e32 v189, v189
	v_lshlrev_b32_e32 v5, 16, v185
	v_and_b32_e32 v185, 0xffff0000, v185
	v_mul_f32_e32 v4, v4, v5
	v_mul_f32_e32 v185, v189, v185
	v_mul_f32_e32 v16, v16, v4
	v_mul_f32_e32 v17, v17, v185
	v_lshlrev_b32_e32 v4, 16, v194
	v_and_b32_e32 v194, 0xffff0000, v194
	v_rcp_f32_e32 v4, v4
	v_rcp_f32_e32 v194, v194
	v_lshlrev_b32_e32 v5, 16, v190
	v_and_b32_e32 v190, 0xffff0000, v190
	v_mul_f32_e32 v4, v4, v5
	v_mul_f32_e32 v190, v194, v190
	v_mul_f32_e32 v10, v10, v4
	v_mul_f32_e32 v11, v11, v190
	v_lshlrev_b32_e32 v4, 16, v195
	v_and_b32_e32 v195, 0xffff0000, v195
	v_rcp_f32_e32 v4, v4
	v_rcp_f32_e32 v195, v195
	v_lshlrev_b32_e32 v5, 16, v191
	v_and_b32_e32 v191, 0xffff0000, v191
	v_mul_f32_e32 v4, v4, v5
	v_mul_f32_e32 v191, v195, v191
	v_mul_f32_e32 v12, v12, v4
	v_mul_f32_e32 v13, v13, v191
	v_lshlrev_b32_e32 v4, 16, v196
	v_and_b32_e32 v196, 0xffff0000, v196
	v_rcp_f32_e32 v4, v4
	v_rcp_f32_e32 v196, v196
	v_lshlrev_b32_e32 v5, 16, v192
	v_and_b32_e32 v192, 0xffff0000, v192
	v_mul_f32_e32 v4, v4, v5
	v_mul_f32_e32 v192, v196, v192
	v_mul_f32_e32 v6, v6, v4
	v_mul_f32_e32 v7, v7, v192
	v_lshlrev_b32_e32 v4, 16, v197
	v_and_b32_e32 v197, 0xffff0000, v197
	v_rcp_f32_e32 v4, v4
	v_rcp_f32_e32 v197, v197
	v_lshlrev_b32_e32 v5, 16, v193
	v_and_b32_e32 v193, 0xffff0000, v193
	v_mul_f32_e32 v4, v4, v5
	v_mul_f32_e32 v193, v197, v193
	v_mul_f32_e32 v8, v8, v4
	v_mul_f32_e32 v9, v9, v193

; #define PG8_TILE_BEGIN(acc, wr, wc, fr, fq) \
;     _Pragma("unroll") for (int ai = 0; ai < 2; ++ai) _Pragma("unroll") for (int m = 0; m < 4; ++m) _Pragma("unroll") for (int bj = 0; bj < 2; ++bj) { \
;         const int trow = ai * 128 + wr * 64 + m * 16 + fr, tcol = bj * 128 + wc * 32 + 8 * fq; f32x4 v0 = acc[ai][bj][m][0], v1 = acc[ai][bj][m][1];
; __device__ __forceinline__ u32x4 pack8(f32x4 v0, f32x4 v1) { u32x4 w; w.x = cvt_pk_bf16(v0[0], v0[1]); w.y = cvt_pk_bf16(v0[2], v0[3]); w.z = cvt_pk_bf16(v1[0], v1[1]); w.w = cvt_pk_bf16(v1[2], v1[3]); return w; }
;     __device__ __forceinline__ void operator()(const f32x4 (&acc)[2][2][4][2], const pg8::Unit& u, int wr, int wc, int fr, int fq) const {
;         PG8_TILE_BEGIN(acc, wr, wc, fr, fq)
;             const int row = u.pm * 256 + trow, col = u.pn * 256 + tcol;
;             const u32x4 g = *(const u32x4*)(PROJ + (size_t)row * INCP + C_GB + col);
;             v0[0] *= bflo(g.x); v0[1] *= bfhi(g.x); v0[2] *= bflo(g.y); v0[3] *= bfhi(g.y); v1[0] *= bflo(g.z); v1[1] *= bfhi(g.z); v1[2] *= bflo(g.w); v1[3] *= bfhi(g.w);
;             *(u32x4*)(MRG + (size_t)row * DM + col) = pg8::pack8(v0, v1);
;         PG8_TILE_END
;     }
.LBB0_1149:
	v_or_b32_e32 v4, s2, v228
	v_readlane_b32 s2, v253, 54
	v_readlane_b32 s3, v253, 55
	v_add_u32_e32 v136, s19, v226
	v_ashrrev_i32_e32 v5, 31, v4
	v_mov_b64_e32 v[138:139], s[2:3]
	v_mad_i64_i32 v[134:135], s[2:3], v136, s46, v[138:139]
	v_lshl_add_u64 v[146:147], v[134:135], 0, s[16:17]
	v_lshlrev_b64 v[134:135], 1, v[4:5]
	v_lshl_add_u64 v[140:141], v[146:147], 0, v[134:135]
	global_load_dwordx4 v[140:143], v[140:141], off
	v_ashrrev_i32_e32 v137, 31, v136
	v_readlane_b32 s4, v254, 59
	v_lshlrev_b64 v[144:145], 11, v[136:137]
	v_readlane_b32 s5, v254, 60
	v_or_b32_e32 v4, 0x80, v4
	v_ashrrev_i32_e32 v5, 31, v4
	v_lshlrev_b64 v[4:5], 1, v[4:5]
	s_and_b64 vcc, exec, s[0:1]
	s_mov_b32 s59, s64
	v_lshl_add_u64 v[150:151], v[146:147], 0, v[4:5]
	global_load_dwordx4 v[150:153], v[150:151], off
	v_or_b32_e32 v148, 16, v136
	v_mad_i64_i32 v[148:149], s[2:3], v148, s46, v[138:139]
	v_lshl_add_u64 v[148:149], v[148:149], 0, s[16:17]
	v_lshl_add_u64 v[154:155], v[148:149], 0, v[134:135]
	global_load_dwordx4 v[154:157], v[154:155], off
	v_lshl_add_u64 v[158:159], v[148:149], 0, v[4:5]
	global_load_dwordx4 v[158:161], v[158:159], off
	v_or_b32_e32 v148, 32, v136
	v_mad_i64_i32 v[148:149], s[2:3], v148, s46, v[138:139]
	v_lshl_add_u64 v[148:149], v[148:149], 0, s[16:17]
	v_lshl_add_u64 v[162:163], v[148:149], 0, v[134:135]
	global_load_dwordx4 v[162:165], v[162:163], off
	v_lshl_add_u64 v[166:167], v[148:149], 0, v[4:5]
	global_load_dwordx4 v[166:169], v[166:167], off
	v_or_b32_e32 v148, 48, v136
	v_mad_i64_i32 v[148:149], s[2:3], v148, s46, v[138:139]
	v_lshl_add_u64 v[148:149], v[148:149], 0, s[16:17]
	v_lshl_add_u64 v[170:171], v[148:149], 0, v[134:135]
	global_load_dwordx4 v[170:173], v[170:171], off
	v_lshl_add_u64 v[174:175], v[148:149], 0, v[4:5]
	global_load_dwordx4 v[174:177], v[174:175], off
	v_mov_b32_e32 v148, v136
	v_ashrrev_i32_e32 v149, 31, v148
	v_lshlrev_b64 v[148:149], 11, v[148:149]
	v_lshl_add_u64 v[146:147], s[4:5], 0, v[148:149]
	v_lshl_add_u64 v[146:147], v[146:147], 0, v[134:135]
	s_waitcnt vmcnt(7)
	v_lshlrev_b32_e32 v186, 16, v140
	v_and_b32_e32 v140, 0xffff0000, v140
	v_mul_f32_e32 v130, v130, v186
	v_mul_f32_e32 v131, v131, v140
	v_lshlrev_b32_e32 v186, 16, v141
	v_and_b32_e32 v141, 0xffff0000, v141
	v_mul_f32_e32 v132, v132, v186
	v_mul_f32_e32 v133, v133, v141
	v_lshlrev_b32_e32 v186, 16, v142
	v_and_b32_e32 v142, 0xffff0000, v142
	v_mul_f32_e32 v182, v126, v186
	v_mul_f32_e32 v183, v127, v142
	v_lshlrev_b32_e32 v186, 16, v143
	v_and_b32_e32 v143, 0xffff0000, v143
	v_mul_f32_e32 v184, v128, v186
	v_mul_f32_e32 v185, v129, v143
	v_cvt_pk_bf16_f32 v126, v130, v131
	v_cvt_pk_bf16_f32 v127, v132, v133
	v_cvt_pk_bf16_f32 v128, v182, v183
	v_cvt_pk_bf16_f32 v129, v184, v185
	global_store_dwordx4 v[146:147], v[126:129], off
	s_waitcnt vmcnt(7)
	v_lshlrev_b32_e32 v186, 16, v150
	v_and_b32_e32 v150, 0xffff0000, v150
	v_mul_f32_e32 v122, v122, v186
	v_mul_f32_e32 v123, v123, v150
	v_lshlrev_b32_e32 v186, 16, v151
	v_and_b32_e32 v151, 0xffff0000, v151
	v_mul_f32_e32 v124, v124, v186
	v_mul_f32_e32 v125, v125, v151
	v_lshlrev_b32_e32 v186, 16, v152
	v_and_b32_e32 v152, 0xffff0000, v152
	v_mul_f32_e32 v182, v118, v186
	v_mul_f32_e32 v183, v119, v152
	v_lshlrev_b32_e32 v186, 16, v153
	v_and_b32_e32 v153, 0xffff0000, v153
	v_mul_f32_e32 v184, v120, v186
	v_mul_f32_e32 v185, v121, v153
	v_cvt_pk_bf16_f32 v118, v122, v123
	v_cvt_pk_bf16_f32 v119, v124, v125
	v_cvt_pk_bf16_f32 v120, v182, v183
	v_cvt_pk_bf16_f32 v121, v184, v185
	global_store_dwordx4 v[146:147], v[118:121], off offset:256
	v_or_b32_e32 v148, 16, v136
	v_ashrrev_i32_e32 v149, 31, v148
	v_lshlrev_b64 v[148:149], 11, v[148:149]
	v_lshl_add_u64 v[146:147], s[4:5], 0, v[148:149]
	v_lshl_add_u64 v[146:147], v[146:147], 0, v[134:135]
	s_waitcnt vmcnt(7)
	v_lshlrev_b32_e32 v186, 16, v154
	v_and_b32_e32 v154, 0xffff0000, v154
	v_mul_f32_e32 v114, v114, v186
	v_mul_f32_e32 v115, v115, v154
	v_lshlrev_b32_e32 v186, 16, v155
	v_and_b32_e32 v155, 0xffff0000, v155
	v_mul_f32_e32 v116, v116, v186
	v_mul_f32_e32 v117, v117, v155
	v_lshlrev_b32_e32 v186, 16, v156
	v_and_b32_e32 v156, 0xffff0000, v156
	v_mul_f32_e32 v182, v110, v186
	v_mul_f32_e32 v183, v111, v156
	v_lshlrev_b32_e32 v186, 16, v157
	v_and_b32_e32 v157, 0xffff0000, v157
	v_mul_f32_e32 v184, v112, v186
	v_mul_f32_e32 v185, v113, v157
	v_cvt_pk_bf16_f32 v110, v114, v115
	v_cvt_pk_bf16_f32 v111, v116, v117
	v_cvt_pk_bf16_f32 v112, v182, v183
	v_cvt_pk_bf16_f32 v113, v184, v185
	global_store_dwordx4 v[146:147], v[110:113], off
	s_waitcnt vmcnt(7)
	v_lshlrev_b32_e32 v186, 16, v158
	v_and_b32_e32 v158, 0xffff0000, v158
	v_mul_f32_e32 v106, v106, v186
	v_mul_f32_e32 v107, v107, v158
	v_lshlrev_b32_e32 v186, 16, v159
	v_and_b32_e32 v159, 0xffff0000, v159
	v_mul_f32_e32 v108, v108, v186
	v_mul_f32_e32 v109, v109, v159
	v_lshlrev_b32_e32 v186, 16, v160
	v_and_b32_e32 v160, 0xffff0000, v160
	v_mul_f32_e32 v182, v102, v186
	v_mul_f32_e32 v183, v103, v160
	v_lshlrev_b32_e32 v186, 16, v161
	v_and_b32_e32 v161, 0xffff0000, v161
	v_mul_f32_e32 v184, v104, v186
	v_mul_f32_e32 v185, v105, v161
	v_cvt_pk_bf16_f32 v102, v106, v107
	v_cvt_pk_bf16_f32 v103, v108, v109
	v_cvt_pk_bf16_f32 v104, v182, v183
	v_cvt_pk_bf16_f32 v105, v184, v185
	global_store_dwordx4 v[146:147], v[102:105], off offset:256
	v_or_b32_e32 v148, 32, v136
	v_ashrrev_i32_e32 v149, 31, v148
	v_lshlrev_b64 v[148:149], 11, v[148:149]
	v_lshl_add_u64 v[146:147], s[4:5], 0, v[148:149]
	v_lshl_add_u64 v[146:147], v[146:147], 0, v[134:135]
	s_waitcnt vmcnt(7)
; #define PG8_TILE_BEGIN(acc, wr, wc, fr, fq) \
;     _Pragma("unroll") for (int ai = 0; ai < 2; ++ai) _Pragma("unroll") for (int m = 0; m < 4; ++m) _Pragma("unroll") for (int bj = 0; bj < 2; ++bj) { \
;         const int trow = ai * 128 + wr * 64 + m * 16 + fr, tcol = bj * 128 + wc * 32 + 8 * fq; f32x4 v0 = acc[ai][bj][m][0], v1 = acc[ai][bj][m][1];
; __device__ __forceinline__ u32x4 pack8(f32x4 v0, f32x4 v1) { u32x4 w; w.x = cvt_pk_bf16(v0[0], v0[1]); w.y = cvt_pk_bf16(v0[2], v0[3]); w.z = cvt_pk_bf16(v1[0], v1[1]); w.w = cvt_pk_bf16(v1[2], v1[3]); return w; }
;     __device__ __forceinline__ void operator()(const f32x4 (&acc)[2][2][4][2], const pg8::Unit& u, int wr, int wc, int fr, int fq) const {
;         PG8_TILE_BEGIN(acc, wr, wc, fr, fq)
;             const int row = u.pm * 256 + trow, col = u.pn * 256 + tcol;
;             const u32x4 g = *(const u32x4*)(PROJ + (size_t)row * INCP + C_GB + col);
;             v0[0] *= bflo(g.x); v0[1] *= bfhi(g.x); v0[2] *= bflo(g.y); v0[3] *= bfhi(g.y); v1[0] *= bflo(g.z); v1[1] *= bfhi(g.z); v1[2] *= bflo(g.w); v1[3] *= bfhi(g.w);
;             *(u32x4*)(MRG + (size_t)row * DM + col) = pg8::pack8(v0, v1);
;         PG8_TILE_END
;     }
	v_lshlrev_b32_e32 v186, 16, v162
	v_and_b32_e32 v162, 0xffff0000, v162
	v_mul_f32_e32 v98, v98, v186
	v_mul_f32_e32 v99, v99, v162
	v_lshlrev_b32_e32 v186, 16, v163
	v_and_b32_e32 v163, 0xffff0000, v163
	v_mul_f32_e32 v100, v100, v186
	v_mul_f32_e32 v101, v101, v163
	v_lshlrev_b32_e32 v186, 16, v164
	v_and_b32_e32 v164, 0xffff0000, v164
	v_mul_f32_e32 v182, v94, v186
	v_mul_f32_e32 v183, v95, v164
	v_lshlrev_b32_e32 v186, 16, v165
	v_and_b32_e32 v165, 0xffff0000, v165
	v_mul_f32_e32 v184, v96, v186
	v_mul_f32_e32 v185, v97, v165
	v_cvt_pk_bf16_f32 v94, v98, v99
	v_cvt_pk_bf16_f32 v95, v100, v101
	v_cvt_pk_bf16_f32 v96, v182, v183
	v_cvt_pk_bf16_f32 v97, v184, v185
	global_store_dwordx4 v[146:147], v[94:97], off
	s_waitcnt vmcnt(7)
	v_lshlrev_b32_e32 v186, 16, v166
	v_and_b32_e32 v166, 0xffff0000, v166
	v_mul_f32_e32 v90, v90, v186
	v_mul_f32_e32 v91, v91, v166
	v_lshlrev_b32_e32 v186, 16, v167
	v_and_b32_e32 v167, 0xffff0000, v167
	v_mul_f32_e32 v92, v92, v186
	v_mul_f32_e32 v93, v93, v167
	v_lshlrev_b32_e32 v186, 16, v168
	v_and_b32_e32 v168, 0xffff0000, v168
	v_mul_f32_e32 v182, v86, v186
	v_mul_f32_e32 v183, v87, v168
	v_lshlrev_b32_e32 v186, 16, v169
	v_and_b32_e32 v169, 0xffff0000, v169
	v_mul_f32_e32 v184, v88, v186
	v_mul_f32_e32 v185, v89, v169
	v_cvt_pk_bf16_f32 v86, v90, v91
	v_cvt_pk_bf16_f32 v87, v92, v93
	v_cvt_pk_bf16_f32 v88, v182, v183
	v_cvt_pk_bf16_f32 v89, v184, v185
	global_store_dwordx4 v[146:147], v[86:89], off offset:256
	v_or_b32_e32 v148, 48, v136
	v_ashrrev_i32_e32 v149, 31, v148
	v_lshlrev_b64 v[148:149], 11, v[148:149]
	v_lshl_add_u64 v[146:147], s[4:5], 0, v[148:149]
	v_lshl_add_u64 v[146:147], v[146:147], 0, v[134:135]
	s_waitcnt vmcnt(7)
	v_lshlrev_b32_e32 v186, 16, v170
	v_and_b32_e32 v170, 0xffff0000, v170
	v_mul_f32_e32 v82, v82, v186
	v_mul_f32_e32 v83, v83, v170
	v_lshlrev_b32_e32 v186, 16, v171
	v_and_b32_e32 v171, 0xffff0000, v171
	v_mul_f32_e32 v84, v84, v186
	v_mul_f32_e32 v85, v85, v171
	v_lshlrev_b32_e32 v186, 16, v172
	v_and_b32_e32 v172, 0xffff0000, v172
	v_mul_f32_e32 v182, v78, v186
	v_mul_f32_e32 v183, v79, v172
	v_lshlrev_b32_e32 v186, 16, v173
	v_and_b32_e32 v173, 0xffff0000, v173
	v_mul_f32_e32 v184, v80, v186
	v_mul_f32_e32 v185, v81, v173
	v_cvt_pk_bf16_f32 v78, v82, v83
	v_cvt_pk_bf16_f32 v79, v84, v85
	v_cvt_pk_bf16_f32 v80, v182, v183
	v_cvt_pk_bf16_f32 v81, v184, v185
	global_store_dwordx4 v[146:147], v[78:81], off
	s_waitcnt vmcnt(7)
	v_lshlrev_b32_e32 v186, 16, v174
	v_and_b32_e32 v174, 0xffff0000, v174
	v_mul_f32_e32 v74, v74, v186
	v_mul_f32_e32 v75, v75, v174
	v_lshlrev_b32_e32 v186, 16, v175
	v_and_b32_e32 v175, 0xffff0000, v175
	v_mul_f32_e32 v76, v76, v186
	v_mul_f32_e32 v77, v77, v175
	v_lshlrev_b32_e32 v186, 16, v176
	v_and_b32_e32 v176, 0xffff0000, v176
	v_mul_f32_e32 v182, v70, v186
	v_mul_f32_e32 v183, v71, v176
	v_lshlrev_b32_e32 v186, 16, v177
	v_and_b32_e32 v177, 0xffff0000, v177
	v_mul_f32_e32 v184, v72, v186
	v_mul_f32_e32 v185, v73, v177
	v_cvt_pk_bf16_f32 v70, v74, v75
	v_cvt_pk_bf16_f32 v71, v76, v77
	v_cvt_pk_bf16_f32 v72, v182, v183
	v_cvt_pk_bf16_f32 v73, v184, v185
	global_store_dwordx4 v[146:147], v[70:73], off offset:256
	v_or_b32_e32 v148, 128, v136
	v_mad_i64_i32 v[148:149], s[2:3], v148, s46, v[138:139]
	v_lshl_add_u64 v[148:149], v[148:149], 0, s[16:17]
	v_lshl_add_u64 v[150:151], v[148:149], 0, v[134:135]
	global_load_dwordx4 v[150:153], v[150:151], off
	v_lshl_add_u64 v[154:155], v[148:149], 0, v[4:5]
	global_load_dwordx4 v[154:157], v[154:155], off
	v_or_b32_e32 v148, 144, v136
	v_mad_i64_i32 v[148:149], s[2:3], v148, s46, v[138:139]
	v_lshl_add_u64 v[148:149], v[148:149], 0, s[16:17]
	v_lshl_add_u64 v[158:159], v[148:149], 0, v[134:135]
	global_load_dwordx4 v[158:161], v[158:159], off
	v_lshl_add_u64 v[162:163], v[148:149], 0, v[4:5]
	global_load_dwordx4 v[162:165], v[162:163], off
	v_or_b32_e32 v148, 160, v136
	v_mad_i64_i32 v[148:149], s[2:3], v148, s46, v[138:139]
	v_lshl_add_u64 v[148:149], v[148:149], 0, s[16:17]
	v_lshl_add_u64 v[166:167], v[148:149], 0, v[134:135]
	global_load_dwordx4 v[166:169], v[166:167], off
	v_lshl_add_u64 v[170:171], v[148:149], 0, v[4:5]
	global_load_dwordx4 v[170:173], v[170:171], off
	v_or_b32_e32 v148, 176, v136
	v_mad_i64_i32 v[148:149], s[2:3], v148, s46, v[138:139]
	v_lshl_add_u64 v[148:149], v[148:149], 0, s[16:17]
	v_lshl_add_u64 v[174:175], v[148:149], 0, v[134:135]
	global_load_dwordx4 v[174:177], v[174:175], off
	v_lshl_add_u64 v[178:179], v[148:149], 0, v[4:5]
	global_load_dwordx4 v[178:181], v[178:179], off
	v_or_b32_e32 v148, 128, v136
	v_ashrrev_i32_e32 v149, 31, v148
	v_lshlrev_b64 v[148:149], 11, v[148:149]
	v_lshl_add_u64 v[146:147], s[4:5], 0, v[148:149]
	v_lshl_add_u64 v[146:147], v[146:147], 0, v[134:135]
	s_waitcnt vmcnt(7)
	v_lshlrev_b32_e32 v186, 16, v150
	v_and_b32_e32 v150, 0xffff0000, v150
	v_mul_f32_e32 v66, v66, v186
	v_mul_f32_e32 v67, v67, v150
	v_lshlrev_b32_e32 v186, 16, v151
	v_and_b32_e32 v151, 0xffff0000, v151
	v_mul_f32_e32 v68, v68, v186
	v_mul_f32_e32 v69, v69, v151
	v_lshlrev_b32_e32 v186, 16, v152
	v_and_b32_e32 v152, 0xffff0000, v152
	v_mul_f32_e32 v182, v62, v186
	v_mul_f32_e32 v183, v63, v152
	v_lshlrev_b32_e32 v186, 16, v153
	v_and_b32_e32 v153, 0xffff0000, v153
	v_mul_f32_e32 v184, v64, v186
	v_mul_f32_e32 v185, v65, v153
	v_cvt_pk_bf16_f32 v62, v66, v67
	v_cvt_pk_bf16_f32 v63, v68, v69
	v_cvt_pk_bf16_f32 v64, v182, v183
	v_cvt_pk_bf16_f32 v65, v184, v185
	global_store_dwordx4 v[146:147], v[62:65], off
	s_waitcnt vmcnt(7)
; #define PG8_TILE_BEGIN(acc, wr, wc, fr, fq) \
;     _Pragma("unroll") for (int ai = 0; ai < 2; ++ai) _Pragma("unroll") for (int m = 0; m < 4; ++m) _Pragma("unroll") for (int bj = 0; bj < 2; ++bj) { \
;         const int trow = ai * 128 + wr * 64 + m * 16 + fr, tcol = bj * 128 + wc * 32 + 8 * fq; f32x4 v0 = acc[ai][bj][m][0], v1 = acc[ai][bj][m][1];
; __device__ __forceinline__ u32x4 pack8(f32x4 v0, f32x4 v1) { u32x4 w; w.x = cvt_pk_bf16(v0[0], v0[1]); w.y = cvt_pk_bf16(v0[2], v0[3]); w.z = cvt_pk_bf16(v1[0], v1[1]); w.w = cvt_pk_bf16(v1[2], v1[3]); return w; }
;     __device__ __forceinline__ void operator()(const f32x4 (&acc)[2][2][4][2], const pg8::Unit& u, int wr, int wc, int fr, int fq) const {
;         PG8_TILE_BEGIN(acc, wr, wc, fr, fq)
;             const int row = u.pm * 256 + trow, col = u.pn * 256 + tcol;
;             const u32x4 g = *(const u32x4*)(PROJ + (size_t)row * INCP + C_GB + col);
;             v0[0] *= bflo(g.x); v0[1] *= bfhi(g.x); v0[2] *= bflo(g.y); v0[3] *= bfhi(g.y); v1[0] *= bflo(g.z); v1[1] *= bfhi(g.z); v1[2] *= bflo(g.w); v1[3] *= bfhi(g.w);
;             *(u32x4*)(MRG + (size_t)row * DM + col) = pg8::pack8(v0, v1);
;         PG8_TILE_END
;     }
	v_lshlrev_b32_e32 v186, 16, v154
	v_and_b32_e32 v154, 0xffff0000, v154
	v_mul_f32_e32 v58, v58, v186
	v_mul_f32_e32 v59, v59, v154
	v_lshlrev_b32_e32 v186, 16, v155
	v_and_b32_e32 v155, 0xffff0000, v155
	v_mul_f32_e32 v60, v60, v186
	v_mul_f32_e32 v61, v61, v155
	v_lshlrev_b32_e32 v186, 16, v156
	v_and_b32_e32 v156, 0xffff0000, v156
	v_mul_f32_e32 v182, v54, v186
	v_mul_f32_e32 v183, v55, v156
	v_lshlrev_b32_e32 v186, 16, v157
	v_and_b32_e32 v157, 0xffff0000, v157
	v_mul_f32_e32 v184, v56, v186
	v_mul_f32_e32 v185, v57, v157
	v_cvt_pk_bf16_f32 v54, v58, v59
	v_cvt_pk_bf16_f32 v55, v60, v61
	v_cvt_pk_bf16_f32 v56, v182, v183
	v_cvt_pk_bf16_f32 v57, v184, v185
	global_store_dwordx4 v[146:147], v[54:57], off offset:256
	v_or_b32_e32 v148, 144, v136
	v_ashrrev_i32_e32 v149, 31, v148
	v_lshlrev_b64 v[148:149], 11, v[148:149]
	v_lshl_add_u64 v[146:147], s[4:5], 0, v[148:149]
	v_lshl_add_u64 v[146:147], v[146:147], 0, v[134:135]
	s_waitcnt vmcnt(7)
	v_lshlrev_b32_e32 v186, 16, v158
	v_and_b32_e32 v158, 0xffff0000, v158
	v_mul_f32_e32 v50, v50, v186
	v_mul_f32_e32 v51, v51, v158
	v_lshlrev_b32_e32 v186, 16, v159
	v_and_b32_e32 v159, 0xffff0000, v159
	v_mul_f32_e32 v52, v52, v186
	v_mul_f32_e32 v53, v53, v159
	v_lshlrev_b32_e32 v186, 16, v160
	v_and_b32_e32 v160, 0xffff0000, v160
	v_mul_f32_e32 v182, v46, v186
	v_mul_f32_e32 v183, v47, v160
	v_lshlrev_b32_e32 v186, 16, v161
	v_and_b32_e32 v161, 0xffff0000, v161
	v_mul_f32_e32 v184, v48, v186
	v_mul_f32_e32 v185, v49, v161
	v_cvt_pk_bf16_f32 v46, v50, v51
	v_cvt_pk_bf16_f32 v47, v52, v53
	v_cvt_pk_bf16_f32 v48, v182, v183
	v_cvt_pk_bf16_f32 v49, v184, v185
	global_store_dwordx4 v[146:147], v[46:49], off
	s_waitcnt vmcnt(7)
	v_lshlrev_b32_e32 v186, 16, v162
	v_and_b32_e32 v162, 0xffff0000, v162
	v_mul_f32_e32 v42, v42, v186
	v_mul_f32_e32 v43, v43, v162
	v_lshlrev_b32_e32 v186, 16, v163
	v_and_b32_e32 v163, 0xffff0000, v163
	v_mul_f32_e32 v44, v44, v186
	v_mul_f32_e32 v45, v45, v163
	v_lshlrev_b32_e32 v186, 16, v164
	v_and_b32_e32 v164, 0xffff0000, v164
	v_mul_f32_e32 v182, v38, v186
	v_mul_f32_e32 v183, v39, v164
	v_lshlrev_b32_e32 v186, 16, v165
	v_and_b32_e32 v165, 0xffff0000, v165
	v_mul_f32_e32 v184, v40, v186
	v_mul_f32_e32 v185, v41, v165
	v_cvt_pk_bf16_f32 v38, v42, v43
	v_cvt_pk_bf16_f32 v39, v44, v45
	v_cvt_pk_bf16_f32 v40, v182, v183
	v_cvt_pk_bf16_f32 v41, v184, v185
	global_store_dwordx4 v[146:147], v[38:41], off offset:256
	v_or_b32_e32 v148, 160, v136
	v_ashrrev_i32_e32 v149, 31, v148
	v_lshlrev_b64 v[148:149], 11, v[148:149]
	v_lshl_add_u64 v[146:147], s[4:5], 0, v[148:149]
	v_lshl_add_u64 v[146:147], v[146:147], 0, v[134:135]
	s_waitcnt vmcnt(7)
	v_lshlrev_b32_e32 v186, 16, v166
	v_and_b32_e32 v166, 0xffff0000, v166
	v_mul_f32_e32 v34, v34, v186
	v_mul_f32_e32 v35, v35, v166
	v_lshlrev_b32_e32 v186, 16, v167
	v_and_b32_e32 v167, 0xffff0000, v167
	v_mul_f32_e32 v36, v36, v186
	v_mul_f32_e32 v37, v37, v167
	v_lshlrev_b32_e32 v186, 16, v168
	v_and_b32_e32 v168, 0xffff0000, v168
	v_mul_f32_e32 v182, v30, v186
	v_mul_f32_e32 v183, v31, v168
	v_lshlrev_b32_e32 v186, 16, v169
	v_and_b32_e32 v169, 0xffff0000, v169
	v_mul_f32_e32 v184, v32, v186
	v_mul_f32_e32 v185, v33, v169
	v_cvt_pk_bf16_f32 v30, v34, v35
	v_cvt_pk_bf16_f32 v31, v36, v37
	v_cvt_pk_bf16_f32 v32, v182, v183
	v_cvt_pk_bf16_f32 v33, v184, v185
	global_store_dwordx4 v[146:147], v[30:33], off
	s_waitcnt vmcnt(7)
	v_lshlrev_b32_e32 v186, 16, v170
	v_and_b32_e32 v170, 0xffff0000, v170
	v_mul_f32_e32 v26, v26, v186
	v_mul_f32_e32 v27, v27, v170
	v_lshlrev_b32_e32 v186, 16, v171
	v_and_b32_e32 v171, 0xffff0000, v171
	v_mul_f32_e32 v28, v28, v186
	v_mul_f32_e32 v29, v29, v171
	v_lshlrev_b32_e32 v186, 16, v172
	v_and_b32_e32 v172, 0xffff0000, v172
	v_mul_f32_e32 v182, v22, v186
	v_mul_f32_e32 v183, v23, v172
	v_lshlrev_b32_e32 v186, 16, v173
	v_and_b32_e32 v173, 0xffff0000, v173
	v_mul_f32_e32 v184, v24, v186
	v_mul_f32_e32 v185, v25, v173
	v_cvt_pk_bf16_f32 v22, v26, v27
	v_cvt_pk_bf16_f32 v23, v28, v29
	v_cvt_pk_bf16_f32 v24, v182, v183
	v_cvt_pk_bf16_f32 v25, v184, v185
	global_store_dwordx4 v[146:147], v[22:25], off offset:256
	v_or_b32_e32 v148, 176, v136
	v_ashrrev_i32_e32 v149, 31, v148
	v_lshlrev_b64 v[148:149], 11, v[148:149]
	v_lshl_add_u64 v[146:147], s[4:5], 0, v[148:149]
	v_lshl_add_u64 v[146:147], v[146:147], 0, v[134:135]
	s_waitcnt vmcnt(7)
	v_lshlrev_b32_e32 v186, 16, v174
	v_and_b32_e32 v174, 0xffff0000, v174
	v_mul_f32_e32 v18, v18, v186
	v_mul_f32_e32 v19, v19, v174
	v_lshlrev_b32_e32 v186, 16, v175
	v_and_b32_e32 v175, 0xffff0000, v175
	v_mul_f32_e32 v20, v20, v186
	v_mul_f32_e32 v21, v21, v175
	v_lshlrev_b32_e32 v186, 16, v176
	v_and_b32_e32 v176, 0xffff0000, v176
	v_mul_f32_e32 v182, v14, v186
	v_mul_f32_e32 v183, v15, v176
	v_lshlrev_b32_e32 v186, 16, v177
	v_and_b32_e32 v177, 0xffff0000, v177
	v_mul_f32_e32 v184, v16, v186
	v_mul_f32_e32 v185, v17, v177
	v_cvt_pk_bf16_f32 v14, v18, v19
	v_cvt_pk_bf16_f32 v15, v20, v21
	v_cvt_pk_bf16_f32 v16, v182, v183
	v_cvt_pk_bf16_f32 v17, v184, v185
	global_store_dwordx4 v[146:147], v[14:17], off
	s_waitcnt vmcnt(7)
	v_lshlrev_b32_e32 v186, 16, v178
	v_and_b32_e32 v178, 0xffff0000, v178
	v_mul_f32_e32 v10, v10, v186
	v_mul_f32_e32 v11, v11, v178
	v_lshlrev_b32_e32 v186, 16, v179
	v_and_b32_e32 v179, 0xffff0000, v179
	v_mul_f32_e32 v12, v12, v186
	v_mul_f32_e32 v13, v13, v179
	v_lshlrev_b32_e32 v186, 16, v180
	v_and_b32_e32 v180, 0xffff0000, v180
	v_mul_f32_e32 v182, v6, v186
	v_mul_f32_e32 v183, v7, v180
	v_lshlrev_b32_e32 v186, 16, v181
	v_and_b32_e32 v181, 0xffff0000, v181
	v_mul_f32_e32 v184, v8, v186
	v_mul_f32_e32 v185, v9, v181
	v_cvt_pk_bf16_f32 v6, v10, v11
	v_cvt_pk_bf16_f32 v7, v12, v13
	v_cvt_pk_bf16_f32 v8, v182, v183
	v_cvt_pk_bf16_f32 v9, v184, v185
	global_store_dwordx4 v[146:147], v[6:9], off offset:256
	s_mov_b64 s[2:3], -1
	s_cbranch_vccnz .LBB0_1128
	s_andn2_b64 vcc, exec, s[12:13]
	s_cbranch_vccnz .LBB0_1127
	s_barrier
	s_branch .LBB0_1127

;     __device__ __forceinline__ void mid(f32x4 (&acc)[2][2][4][2], const pg8::Unit& u, int wr, int wc, int fr_, int fq) const {
;     ...
;                 for (int bj = 0; bj < 2; ++bj) { const size_t o = (size_t)(u.pm * 256 + ai * 128 + wr * 64 + m * 16 + fr) * INCP + u.pn * 256 + bj * 128 + wc * 32 + 8 * fq;
;                     const u32x4 ga = *(const u32x4*)(PROJ + o + C_GA), gb = *(const u32x4*)(PROJ + o + C_GB);
; #pragma unroll
;                     for (int i = 0; i < 4; ++i) { const float r0 = bflo(ga[i]) * __builtin_amdgcn_rcpf(bflo(gb[i])), r1 = bfhi(ga[i]) * __builtin_amdgcn_rcpf(bfhi(gb[i]));
;                         acc[ai][bj][m][i >> 1][2 * (i & 1)] *= r0; acc[ai][bj][m][i >> 1][2 * (i & 1) + 1] *= r1; }
;                     __builtin_amdgcn_sched_barrier(0); }
.LBB0_3598:
	v_mov_b32_e32 v2, v225
	s_nop 0
	v_add_u32_e32 v2, s44, v2
	v_add_u32_e32 v4, s17, v2
	v_mad_i64_i32 v[4:5], s[26:27], v4, s48, v[212:213]
	v_add_co_u32_e32 v4, vcc, 0x1000, v4
	s_nop 1
	v_addc_co_u32_e32 v5, vcc, 0, v5, vcc
	global_load_dwordx4 v[134:137], v[4:5], off offset:320
	global_load_dwordx4 v[138:141], v[4:5], off offset:2368
	global_load_dwordx4 v[142:145], v[4:5], off offset:576
	global_load_dwordx4 v[146:149], v[4:5], off offset:2624
	v_add_u32_e32 v4, s21, v2
	v_mad_i64_i32 v[4:5], s[26:27], v4, s48, v[212:213]
	v_add_co_u32_e32 v4, vcc, s49, v4
	s_nop 1
	v_addc_co_u32_e32 v5, vcc, 0, v5, vcc
	global_load_dwordx4 v[150:153], v[4:5], off offset:320
	global_load_dwordx4 v[154:157], v[4:5], off offset:2368
	global_load_dwordx4 v[158:161], v[4:5], off offset:576
	global_load_dwordx4 v[162:165], v[4:5], off offset:2624
	v_add_u32_e32 v4, s33, v2
	v_mad_i64_i32 v[4:5], s[26:27], v4, s48, v[212:213]
	v_add_co_u32_e32 v4, vcc, s49, v4
	s_nop 1
	v_addc_co_u32_e32 v5, vcc, 0, v5, vcc
	global_load_dwordx4 v[166:169], v[4:5], off offset:320
	global_load_dwordx4 v[170:173], v[4:5], off offset:2368
	global_load_dwordx4 v[174:177], v[4:5], off offset:576
	global_load_dwordx4 v[178:181], v[4:5], off offset:2624
	v_add_u32_e32 v4, s57, v2
	v_mad_i64_i32 v[4:5], s[26:27], v4, s48, v[212:213]
	v_add_co_u32_e32 v4, vcc, s49, v4
	s_nop 1
	v_addc_co_u32_e32 v5, vcc, 0, v5, vcc
	global_load_dwordx4 v[182:185], v[4:5], off offset:320
	global_load_dwordx4 v[186:189], v[4:5], off offset:2368
	global_load_dwordx4 v[190:193], v[4:5], off offset:576
	global_load_dwordx4 v[194:197], v[4:5], off offset:2624
	s_waitcnt vmcnt(12)
	v_lshlrev_b32_e32 v4, 16, v138
	v_and_b32_e32 v138, 0xffff0000, v138
	v_rcp_f32_e32 v4, v4
	v_rcp_f32_e32 v138, v138
	v_lshlrev_b32_e32 v5, 16, v134
	v_and_b32_e32 v134, 0xffff0000, v134
	v_mul_f32_e32 v4, v4, v5
	v_mul_f32_e32 v134, v138, v134
	v_mul_f32_e32 v130, v130, v4
	v_mul_f32_e32 v131, v131, v134
	v_lshlrev_b32_e32 v4, 16, v139
	v_and_b32_e32 v139, 0xffff0000, v139
	v_rcp_f32_e32 v4, v4
	v_rcp_f32_e32 v139, v139
	v_lshlrev_b32_e32 v5, 16, v135
	v_and_b32_e32 v135, 0xffff0000, v135
	v_mul_f32_e32 v4, v4, v5
	v_mul_f32_e32 v135, v139, v135
	v_mul_f32_e32 v132, v132, v4
	v_mul_f32_e32 v133, v133, v135
	v_lshlrev_b32_e32 v4, 16, v140
	v_and_b32_e32 v140, 0xffff0000, v140
	v_rcp_f32_e32 v4, v4
	v_rcp_f32_e32 v140, v140
	v_lshlrev_b32_e32 v5, 16, v136
	v_and_b32_e32 v136, 0xffff0000, v136
	v_mul_f32_e32 v4, v4, v5
	v_mul_f32_e32 v136, v140, v136
	v_mul_f32_e32 v126, v126, v4
	v_mul_f32_e32 v127, v127, v136
	v_lshlrev_b32_e32 v4, 16, v141
	v_and_b32_e32 v141, 0xffff0000, v141
	v_rcp_f32_e32 v4, v4
	v_rcp_f32_e32 v141, v141
	v_lshlrev_b32_e32 v5, 16, v137
	v_and_b32_e32 v137, 0xffff0000, v137
	v_mul_f32_e32 v4, v4, v5
	v_mul_f32_e32 v137, v141, v137
	v_mul_f32_e32 v128, v128, v4
	v_mul_f32_e32 v129, v129, v137
	v_lshlrev_b32_e32 v4, 16, v146
	v_and_b32_e32 v146, 0xffff0000, v146
	v_rcp_f32_e32 v4, v4
	v_rcp_f32_e32 v146, v146
	v_lshlrev_b32_e32 v5, 16, v142
	v_and_b32_e32 v142, 0xffff0000, v142
	v_mul_f32_e32 v4, v4, v5
	v_mul_f32_e32 v142, v146, v142
	v_mul_f32_e32 v122, v122, v4
	v_mul_f32_e32 v123, v123, v142
	v_lshlrev_b32_e32 v4, 16, v147
	v_and_b32_e32 v147, 0xffff0000, v147
	v_rcp_f32_e32 v4, v4
	v_rcp_f32_e32 v147, v147
	v_lshlrev_b32_e32 v5, 16, v143
	v_and_b32_e32 v143, 0xffff0000, v143
	v_mul_f32_e32 v4, v4, v5
	v_mul_f32_e32 v143, v147, v143
	v_mul_f32_e32 v124, v124, v4
	v_mul_f32_e32 v125, v125, v143
	v_lshlrev_b32_e32 v4, 16, v148
	v_and_b32_e32 v148, 0xffff0000, v148
	v_rcp_f32_e32 v4, v4
	v_rcp_f32_e32 v148, v148
	v_lshlrev_b32_e32 v5, 16, v144
	v_and_b32_e32 v144, 0xffff0000, v144
	v_mul_f32_e32 v4, v4, v5
	v_mul_f32_e32 v144, v148, v144
	v_mul_f32_e32 v118, v118, v4
	v_mul_f32_e32 v119, v119, v144
	v_lshlrev_b32_e32 v4, 16, v149
	v_and_b32_e32 v149, 0xffff0000, v149
	v_rcp_f32_e32 v4, v4
	v_rcp_f32_e32 v149, v149
	v_lshlrev_b32_e32 v5, 16, v145
	v_and_b32_e32 v145, 0xffff0000, v145
	v_mul_f32_e32 v4, v4, v5
	v_mul_f32_e32 v145, v149, v145
	v_mul_f32_e32 v120, v120, v4
	v_mul_f32_e32 v121, v121, v145
	s_waitcnt vmcnt(8)
	v_lshlrev_b32_e32 v4, 16, v154
	v_and_b32_e32 v154, 0xffff0000, v154
	v_rcp_f32_e32 v4, v4
	v_rcp_f32_e32 v154, v154
	v_lshlrev_b32_e32 v5, 16, v150
	v_and_b32_e32 v150, 0xffff0000, v150
	v_mul_f32_e32 v4, v4, v5
	v_mul_f32_e32 v150, v154, v150
	v_mul_f32_e32 v114, v114, v4
	v_mul_f32_e32 v115, v115, v150
	v_lshlrev_b32_e32 v4, 16, v155
	v_and_b32_e32 v155, 0xffff0000, v155
	v_rcp_f32_e32 v4, v4
	v_rcp_f32_e32 v155, v155
	v_lshlrev_b32_e32 v5, 16, v151
	v_and_b32_e32 v151, 0xffff0000, v151
	v_mul_f32_e32 v4, v4, v5
	v_mul_f32_e32 v151, v155, v151
	v_mul_f32_e32 v116, v116, v4
	v_mul_f32_e32 v117, v117, v151
	v_lshlrev_b32_e32 v4, 16, v156
	v_and_b32_e32 v156, 0xffff0000, v156
	v_rcp_f32_e32 v4, v4
	v_rcp_f32_e32 v156, v156
	v_lshlrev_b32_e32 v5, 16, v152
	v_and_b32_e32 v152, 0xffff0000, v152
	v_mul_f32_e32 v4, v4, v5
	v_mul_f32_e32 v152, v156, v152
	v_mul_f32_e32 v110, v110, v4
	v_mul_f32_e32 v111, v111, v152
	v_lshlrev_b32_e32 v4, 16, v157
	v_and_b32_e32 v157, 0xffff0000, v157
	v_rcp_f32_e32 v4, v4
	v_rcp_f32_e32 v157, v157
	v_lshlrev_b32_e32 v5, 16, v153
	v_and_b32_e32 v153, 0xffff0000, v153
	v_mul_f32_e32 v4, v4, v5
	v_mul_f32_e32 v153, v157, v153
	v_mul_f32_e32 v112, v112, v4
	v_mul_f32_e32 v113, v113, v153
	v_lshlrev_b32_e32 v4, 16, v162
	v_and_b32_e32 v162, 0xffff0000, v162
	v_rcp_f32_e32 v4, v4
	v_rcp_f32_e32 v162, v162
	v_lshlrev_b32_e32 v5, 16, v158
	v_and_b32_e32 v158, 0xffff0000, v158
	v_mul_f32_e32 v4, v4, v5
	v_mul_f32_e32 v158, v162, v158
	v_mul_f32_e32 v106, v106, v4
	v_mul_f32_e32 v107, v107, v158
	v_lshlrev_b32_e32 v4, 16, v163
	v_and_b32_e32 v163, 0xffff0000, v163
	v_rcp_f32_e32 v4, v4
	v_rcp_f32_e32 v163, v163
	v_lshlrev_b32_e32 v5, 16, v159
	v_and_b32_e32 v159, 0xffff0000, v159
	v_mul_f32_e32 v4, v4, v5
	v_mul_f32_e32 v159, v163, v159
	v_mul_f32_e32 v108, v108, v4
	v_mul_f32_e32 v109, v109, v159
	v_lshlrev_b32_e32 v4, 16, v164
	v_and_b32_e32 v164, 0xffff0000, v164
	v_rcp_f32_e32 v4, v4
	v_rcp_f32_e32 v164, v164
	v_lshlrev_b32_e32 v5, 16, v160
	v_and_b32_e32 v160, 0xffff0000, v160
	v_mul_f32_e32 v4, v4, v5
	v_mul_f32_e32 v160, v164, v160
	v_mul_f32_e32 v102, v102, v4
	v_mul_f32_e32 v103, v103, v160
	v_lshlrev_b32_e32 v4, 16, v165
	v_and_b32_e32 v165, 0xffff0000, v165
	v_rcp_f32_e32 v4, v4
	v_rcp_f32_e32 v165, v165
	v_lshlrev_b32_e32 v5, 16, v161
	v_and_b32_e32 v161, 0xffff0000, v161
	v_mul_f32_e32 v4, v4, v5
	v_mul_f32_e32 v161, v165, v161
	v_mul_f32_e32 v104, v104, v4
	v_mul_f32_e32 v105, v105, v161
	s_waitcnt vmcnt(4)
;     __device__ __forceinline__ void mid(f32x4 (&acc)[2][2][4][2], const pg8::Unit& u, int wr, int wc, int fr_, int fq) const {
;     ...
;                 for (int bj = 0; bj < 2; ++bj) { const size_t o = (size_t)(u.pm * 256 + ai * 128 + wr * 64 + m * 16 + fr) * INCP + u.pn * 256 + bj * 128 + wc * 32 + 8 * fq;
;                     const u32x4 ga = *(const u32x4*)(PROJ + o + C_GA), gb = *(const u32x4*)(PROJ + o + C_GB);
; #pragma unroll
;                     for (int i = 0; i < 4; ++i) { const float r0 = bflo(ga[i]) * __builtin_amdgcn_rcpf(bflo(gb[i])), r1 = bfhi(ga[i]) * __builtin_amdgcn_rcpf(bfhi(gb[i]));
;                         acc[ai][bj][m][i >> 1][2 * (i & 1)] *= r0; acc[ai][bj][m][i >> 1][2 * (i & 1) + 1] *= r1; }
;                     __builtin_amdgcn_sched_barrier(0); }
	v_lshlrev_b32_e32 v4, 16, v170
	v_and_b32_e32 v170, 0xffff0000, v170
	v_rcp_f32_e32 v4, v4
	v_rcp_f32_e32 v170, v170
	v_lshlrev_b32_e32 v5, 16, v166
	v_and_b32_e32 v166, 0xffff0000, v166
	v_mul_f32_e32 v4, v4, v5
	v_mul_f32_e32 v166, v170, v166
	v_mul_f32_e32 v98, v98, v4
	v_mul_f32_e32 v99, v99, v166
	v_lshlrev_b32_e32 v4, 16, v171
	v_and_b32_e32 v171, 0xffff0000, v171
	v_rcp_f32_e32 v4, v4
	v_rcp_f32_e32 v171, v171
	v_lshlrev_b32_e32 v5, 16, v167
	v_and_b32_e32 v167, 0xffff0000, v167
	v_mul_f32_e32 v4, v4, v5
	v_mul_f32_e32 v167, v171, v167
	v_mul_f32_e32 v100, v100, v4
	v_mul_f32_e32 v101, v101, v167
	v_lshlrev_b32_e32 v4, 16, v172
	v_and_b32_e32 v172, 0xffff0000, v172
	v_rcp_f32_e32 v4, v4
	v_rcp_f32_e32 v172, v172
	v_lshlrev_b32_e32 v5, 16, v168
	v_and_b32_e32 v168, 0xffff0000, v168
	v_mul_f32_e32 v4, v4, v5
	v_mul_f32_e32 v168, v172, v168
	v_mul_f32_e32 v94, v94, v4
	v_mul_f32_e32 v95, v95, v168
	v_lshlrev_b32_e32 v4, 16, v173
	v_and_b32_e32 v173, 0xffff0000, v173
	v_rcp_f32_e32 v4, v4
	v_rcp_f32_e32 v173, v173
	v_lshlrev_b32_e32 v5, 16, v169
	v_and_b32_e32 v169, 0xffff0000, v169
	v_mul_f32_e32 v4, v4, v5
	v_mul_f32_e32 v169, v173, v169
	v_mul_f32_e32 v96, v96, v4
	v_mul_f32_e32 v97, v97, v169
	v_lshlrev_b32_e32 v4, 16, v178
	v_and_b32_e32 v178, 0xffff0000, v178
	v_rcp_f32_e32 v4, v4
	v_rcp_f32_e32 v178, v178
	v_lshlrev_b32_e32 v5, 16, v174
	v_and_b32_e32 v174, 0xffff0000, v174
	v_mul_f32_e32 v4, v4, v5
	v_mul_f32_e32 v174, v178, v174
	v_mul_f32_e32 v90, v90, v4
	v_mul_f32_e32 v91, v91, v174
	v_lshlrev_b32_e32 v4, 16, v179
	v_and_b32_e32 v179, 0xffff0000, v179
	v_rcp_f32_e32 v4, v4
	v_rcp_f32_e32 v179, v179
	v_lshlrev_b32_e32 v5, 16, v175
	v_and_b32_e32 v175, 0xffff0000, v175
	v_mul_f32_e32 v4, v4, v5
	v_mul_f32_e32 v175, v179, v175
	v_mul_f32_e32 v92, v92, v4
	v_mul_f32_e32 v93, v93, v175
	v_lshlrev_b32_e32 v4, 16, v180
	v_and_b32_e32 v180, 0xffff0000, v180
	v_rcp_f32_e32 v4, v4
	v_rcp_f32_e32 v180, v180
	v_lshlrev_b32_e32 v5, 16, v176
	v_and_b32_e32 v176, 0xffff0000, v176
	v_mul_f32_e32 v4, v4, v5
	v_mul_f32_e32 v176, v180, v176
	v_mul_f32_e32 v86, v86, v4
	v_mul_f32_e32 v87, v87, v176
	v_lshlrev_b32_e32 v4, 16, v181
	v_and_b32_e32 v181, 0xffff0000, v181
	v_rcp_f32_e32 v4, v4
	v_rcp_f32_e32 v181, v181
	v_lshlrev_b32_e32 v5, 16, v177
	v_and_b32_e32 v177, 0xffff0000, v177
	v_mul_f32_e32 v4, v4, v5
	v_mul_f32_e32 v177, v181, v177
	v_mul_f32_e32 v88, v88, v4
	v_mul_f32_e32 v89, v89, v177
	s_waitcnt vmcnt(0)
	v_lshlrev_b32_e32 v4, 16, v186
	v_and_b32_e32 v186, 0xffff0000, v186
	v_rcp_f32_e32 v4, v4
	v_rcp_f32_e32 v186, v186
	v_lshlrev_b32_e32 v5, 16, v182
	v_and_b32_e32 v182, 0xffff0000, v182
	v_mul_f32_e32 v4, v4, v5
	v_mul_f32_e32 v182, v186, v182
	v_mul_f32_e32 v82, v82, v4
	v_mul_f32_e32 v83, v83, v182
	v_lshlrev_b32_e32 v4, 16, v187
	v_and_b32_e32 v187, 0xffff0000, v187
	v_rcp_f32_e32 v4, v4
	v_rcp_f32_e32 v187, v187
	v_lshlrev_b32_e32 v5, 16, v183
	v_and_b32_e32 v183, 0xffff0000, v183
	v_mul_f32_e32 v4, v4, v5
	v_mul_f32_e32 v183, v187, v183
	v_mul_f32_e32 v84, v84, v4
	v_mul_f32_e32 v85, v85, v183
	v_lshlrev_b32_e32 v4, 16, v188
	v_and_b32_e32 v188, 0xffff0000, v188
	v_rcp_f32_e32 v4, v4
	v_rcp_f32_e32 v188, v188
	v_lshlrev_b32_e32 v5, 16, v184
	v_and_b32_e32 v184, 0xffff0000, v184
	v_mul_f32_e32 v4, v4, v5
	v_mul_f32_e32 v184, v188, v184
	v_mul_f32_e32 v78, v78, v4
	v_mul_f32_e32 v79, v79, v184
	v_lshlrev_b32_e32 v4, 16, v189
	v_and_b32_e32 v189, 0xffff0000, v189
	v_rcp_f32_e32 v4, v4
	v_rcp_f32_e32 v189, v189
	v_lshlrev_b32_e32 v5, 16, v185
	v_and_b32_e32 v185, 0xffff0000, v185
	v_mul_f32_e32 v4, v4, v5
	v_mul_f32_e32 v185, v189, v185
	v_mul_f32_e32 v80, v80, v4
	v_mul_f32_e32 v81, v81, v185
	v_lshlrev_b32_e32 v4, 16, v194
	v_and_b32_e32 v194, 0xffff0000, v194
	v_rcp_f32_e32 v4, v4
	v_rcp_f32_e32 v194, v194
	v_lshlrev_b32_e32 v5, 16, v190
	v_and_b32_e32 v190, 0xffff0000, v190
	v_mul_f32_e32 v4, v4, v5
	v_mul_f32_e32 v190, v194, v190
	v_mul_f32_e32 v74, v74, v4
	v_mul_f32_e32 v75, v75, v190
	v_lshlrev_b32_e32 v4, 16, v195
	v_and_b32_e32 v195, 0xffff0000, v195
	v_rcp_f32_e32 v4, v4
	v_rcp_f32_e32 v195, v195
	v_lshlrev_b32_e32 v5, 16, v191
	v_and_b32_e32 v191, 0xffff0000, v191
	v_mul_f32_e32 v4, v4, v5
	v_mul_f32_e32 v191, v195, v191
	v_mul_f32_e32 v76, v76, v4
	v_mul_f32_e32 v77, v77, v191
	v_lshlrev_b32_e32 v4, 16, v196
	v_and_b32_e32 v196, 0xffff0000, v196
	v_rcp_f32_e32 v4, v4
	v_rcp_f32_e32 v196, v196
	v_lshlrev_b32_e32 v5, 16, v192
	v_and_b32_e32 v192, 0xffff0000, v192
	v_mul_f32_e32 v4, v4, v5
	v_mul_f32_e32 v192, v196, v192
	v_mul_f32_e32 v70, v70, v4
	v_mul_f32_e32 v71, v71, v192
	v_lshlrev_b32_e32 v4, 16, v197
	v_and_b32_e32 v197, 0xffff0000, v197
	v_rcp_f32_e32 v4, v4
	v_rcp_f32_e32 v197, v197
	v_lshlrev_b32_e32 v5, 16, v193
	v_and_b32_e32 v193, 0xffff0000, v193
	v_mul_f32_e32 v4, v4, v5
	v_mul_f32_e32 v193, v197, v193
	v_mul_f32_e32 v72, v72, v4
	v_mul_f32_e32 v73, v73, v193
	v_add_u32_e32 v4, s58, v2
	v_mad_i64_i32 v[4:5], s[26:27], v4, s48, v[212:213]
	v_add_co_u32_e32 v4, vcc, s49, v4
	s_nop 1
	v_addc_co_u32_e32 v5, vcc, 0, v5, vcc
	global_load_dwordx4 v[134:137], v[4:5], off offset:320
	global_load_dwordx4 v[138:141], v[4:5], off offset:2368
	global_load_dwordx4 v[142:145], v[4:5], off offset:576
	global_load_dwordx4 v[146:149], v[4:5], off offset:2624
	v_add_u32_e32 v4, s59, v2
	v_mad_i64_i32 v[4:5], s[26:27], v4, s48, v[212:213]
	v_add_co_u32_e32 v4, vcc, s49, v4
	s_nop 1
	v_addc_co_u32_e32 v5, vcc, 0, v5, vcc
	global_load_dwordx4 v[150:153], v[4:5], off offset:320
	global_load_dwordx4 v[154:157], v[4:5], off offset:2368
	global_load_dwordx4 v[158:161], v[4:5], off offset:576
	global_load_dwordx4 v[162:165], v[4:5], off offset:2624
	v_add_u32_e32 v4, s60, v2
	v_mad_i64_i32 v[4:5], s[26:27], v4, s48, v[212:213]
	v_add_co_u32_e32 v4, vcc, s49, v4
	s_nop 1
	v_addc_co_u32_e32 v5, vcc, 0, v5, vcc
	global_load_dwordx4 v[166:169], v[4:5], off offset:320
	global_load_dwordx4 v[170:173], v[4:5], off offset:2368
	global_load_dwordx4 v[174:177], v[4:5], off offset:576
	global_load_dwordx4 v[178:181], v[4:5], off offset:2624
	v_add_u32_e32 v2, s61, v2
	v_mad_i64_i32 v[4:5], s[26:27], v2, s48, v[212:213]
	v_add_co_u32_e32 v4, vcc, s49, v4
	s_nop 1
	v_addc_co_u32_e32 v5, vcc, 0, v5, vcc
	global_load_dwordx4 v[182:185], v[4:5], off offset:320
	global_load_dwordx4 v[186:189], v[4:5], off offset:2368
	global_load_dwordx4 v[190:193], v[4:5], off offset:576
	global_load_dwordx4 v[194:197], v[4:5], off offset:2624
	s_waitcnt vmcnt(12)
;     __device__ __forceinline__ void mid(f32x4 (&acc)[2][2][4][2], const pg8::Unit& u, int wr, int wc, int fr_, int fq) const {
;     ...
;                 for (int bj = 0; bj < 2; ++bj) { const size_t o = (size_t)(u.pm * 256 + ai * 128 + wr * 64 + m * 16 + fr) * INCP + u.pn * 256 + bj * 128 + wc * 32 + 8 * fq;
;                     const u32x4 ga = *(const u32x4*)(PROJ + o + C_GA), gb = *(const u32x4*)(PROJ + o + C_GB);
; #pragma unroll
;                     for (int i = 0; i < 4; ++i) { const float r0 = bflo(ga[i]) * __builtin_amdgcn_rcpf(bflo(gb[i])), r1 = bfhi(ga[i]) * __builtin_amdgcn_rcpf(bfhi(gb[i]));
;                         acc[ai][bj][m][i >> 1][2 * (i & 1)] *= r0; acc[ai][bj][m][i >> 1][2 * (i & 1) + 1] *= r1; }
;                     __builtin_amdgcn_sched_barrier(0); }
	v_lshlrev_b32_e32 v4, 16, v138
	v_and_b32_e32 v138, 0xffff0000, v138
	v_rcp_f32_e32 v4, v4
	v_rcp_f32_e32 v138, v138
	v_lshlrev_b32_e32 v5, 16, v134
	v_and_b32_e32 v134, 0xffff0000, v134
	v_mul_f32_e32 v4, v4, v5
	v_mul_f32_e32 v134, v138, v134
	v_mul_f32_e32 v66, v66, v4
	v_mul_f32_e32 v67, v67, v134
	v_lshlrev_b32_e32 v4, 16, v139
	v_and_b32_e32 v139, 0xffff0000, v139
	v_rcp_f32_e32 v4, v4
	v_rcp_f32_e32 v139, v139
	v_lshlrev_b32_e32 v5, 16, v135
	v_and_b32_e32 v135, 0xffff0000, v135
	v_mul_f32_e32 v4, v4, v5
	v_mul_f32_e32 v135, v139, v135
	v_mul_f32_e32 v68, v68, v4
	v_mul_f32_e32 v69, v69, v135
	v_lshlrev_b32_e32 v4, 16, v140
	v_and_b32_e32 v140, 0xffff0000, v140
	v_rcp_f32_e32 v4, v4
	v_rcp_f32_e32 v140, v140
	v_lshlrev_b32_e32 v5, 16, v136
	v_and_b32_e32 v136, 0xffff0000, v136
	v_mul_f32_e32 v4, v4, v5
	v_mul_f32_e32 v136, v140, v136
	v_mul_f32_e32 v62, v62, v4
	v_mul_f32_e32 v63, v63, v136
	v_lshlrev_b32_e32 v4, 16, v141
	v_and_b32_e32 v141, 0xffff0000, v141
	v_rcp_f32_e32 v4, v4
	v_rcp_f32_e32 v141, v141
	v_lshlrev_b32_e32 v5, 16, v137
	v_and_b32_e32 v137, 0xffff0000, v137
	v_mul_f32_e32 v4, v4, v5
	v_mul_f32_e32 v137, v141, v137
	v_mul_f32_e32 v64, v64, v4
	v_mul_f32_e32 v65, v65, v137
	v_lshlrev_b32_e32 v4, 16, v146
	v_and_b32_e32 v146, 0xffff0000, v146
	v_rcp_f32_e32 v4, v4
	v_rcp_f32_e32 v146, v146
	v_lshlrev_b32_e32 v5, 16, v142
	v_and_b32_e32 v142, 0xffff0000, v142
	v_mul_f32_e32 v4, v4, v5
	v_mul_f32_e32 v142, v146, v142
	v_mul_f32_e32 v58, v58, v4
	v_mul_f32_e32 v59, v59, v142
	v_lshlrev_b32_e32 v4, 16, v147
	v_and_b32_e32 v147, 0xffff0000, v147
	v_rcp_f32_e32 v4, v4
	v_rcp_f32_e32 v147, v147
	v_lshlrev_b32_e32 v5, 16, v143
	v_and_b32_e32 v143, 0xffff0000, v143
	v_mul_f32_e32 v4, v4, v5
	v_mul_f32_e32 v143, v147, v143
	v_mul_f32_e32 v60, v60, v4
	v_mul_f32_e32 v61, v61, v143
	v_lshlrev_b32_e32 v4, 16, v148
	v_and_b32_e32 v148, 0xffff0000, v148
	v_rcp_f32_e32 v4, v4
	v_rcp_f32_e32 v148, v148
	v_lshlrev_b32_e32 v5, 16, v144
	v_and_b32_e32 v144, 0xffff0000, v144
	v_mul_f32_e32 v4, v4, v5
	v_mul_f32_e32 v144, v148, v144
	v_mul_f32_e32 v54, v54, v4
	v_mul_f32_e32 v55, v55, v144
	v_lshlrev_b32_e32 v4, 16, v149
	v_and_b32_e32 v149, 0xffff0000, v149
	v_rcp_f32_e32 v4, v4
	v_rcp_f32_e32 v149, v149
	v_lshlrev_b32_e32 v5, 16, v145
	v_and_b32_e32 v145, 0xffff0000, v145
	v_mul_f32_e32 v4, v4, v5
	v_mul_f32_e32 v145, v149, v145
	v_mul_f32_e32 v56, v56, v4
	v_mul_f32_e32 v57, v57, v145
	s_waitcnt vmcnt(8)
	v_lshlrev_b32_e32 v4, 16, v154
	v_and_b32_e32 v154, 0xffff0000, v154
	v_rcp_f32_e32 v4, v4
	v_rcp_f32_e32 v154, v154
	v_lshlrev_b32_e32 v5, 16, v150
	v_and_b32_e32 v150, 0xffff0000, v150
	v_mul_f32_e32 v4, v4, v5
	v_mul_f32_e32 v150, v154, v150
	v_mul_f32_e32 v50, v50, v4
	v_mul_f32_e32 v51, v51, v150
	v_lshlrev_b32_e32 v4, 16, v155
	v_and_b32_e32 v155, 0xffff0000, v155
	v_rcp_f32_e32 v4, v4
	v_rcp_f32_e32 v155, v155
	v_lshlrev_b32_e32 v5, 16, v151
	v_and_b32_e32 v151, 0xffff0000, v151
	v_mul_f32_e32 v4, v4, v5
	v_mul_f32_e32 v151, v155, v151
	v_mul_f32_e32 v52, v52, v4
	v_mul_f32_e32 v53, v53, v151
	v_lshlrev_b32_e32 v4, 16, v156
	v_and_b32_e32 v156, 0xffff0000, v156
	v_rcp_f32_e32 v4, v4
	v_rcp_f32_e32 v156, v156
	v_lshlrev_b32_e32 v5, 16, v152
	v_and_b32_e32 v152, 0xffff0000, v152
	v_mul_f32_e32 v4, v4, v5
	v_mul_f32_e32 v152, v156, v152
	v_mul_f32_e32 v46, v46, v4
	v_mul_f32_e32 v47, v47, v152
	v_lshlrev_b32_e32 v4, 16, v157
	v_and_b32_e32 v157, 0xffff0000, v157
	v_rcp_f32_e32 v4, v4
	v_rcp_f32_e32 v157, v157
	v_lshlrev_b32_e32 v5, 16, v153
	v_and_b32_e32 v153, 0xffff0000, v153
	v_mul_f32_e32 v4, v4, v5
	v_mul_f32_e32 v153, v157, v153
	v_mul_f32_e32 v48, v48, v4
	v_mul_f32_e32 v49, v49, v153
	v_lshlrev_b32_e32 v4, 16, v162
	v_and_b32_e32 v162, 0xffff0000, v162
	v_rcp_f32_e32 v4, v4
	v_rcp_f32_e32 v162, v162
	v_lshlrev_b32_e32 v5, 16, v158
	v_and_b32_e32 v158, 0xffff0000, v158
	v_mul_f32_e32 v4, v4, v5
	v_mul_f32_e32 v158, v162, v158
	v_mul_f32_e32 v42, v42, v4
	v_mul_f32_e32 v43, v43, v158
	v_lshlrev_b32_e32 v4, 16, v163
	v_and_b32_e32 v163, 0xffff0000, v163
	v_rcp_f32_e32 v4, v4
	v_rcp_f32_e32 v163, v163
	v_lshlrev_b32_e32 v5, 16, v159
	v_and_b32_e32 v159, 0xffff0000, v159
	v_mul_f32_e32 v4, v4, v5
	v_mul_f32_e32 v159, v163, v159
	v_mul_f32_e32 v44, v44, v4
	v_mul_f32_e32 v45, v45, v159
	v_lshlrev_b32_e32 v4, 16, v164
	v_and_b32_e32 v164, 0xffff0000, v164
	v_rcp_f32_e32 v4, v4
	v_rcp_f32_e32 v164, v164
	v_lshlrev_b32_e32 v5, 16, v160
	v_and_b32_e32 v160, 0xffff0000, v160
	v_mul_f32_e32 v4, v4, v5
	v_mul_f32_e32 v160, v164, v160
	v_mul_f32_e32 v38, v38, v4
	v_mul_f32_e32 v39, v39, v160
	v_lshlrev_b32_e32 v4, 16, v165
	v_and_b32_e32 v165, 0xffff0000, v165
	v_rcp_f32_e32 v4, v4
	v_rcp_f32_e32 v165, v165
	v_lshlrev_b32_e32 v5, 16, v161
	v_and_b32_e32 v161, 0xffff0000, v161
	v_mul_f32_e32 v4, v4, v5
	v_mul_f32_e32 v161, v165, v161
	v_mul_f32_e32 v40, v40, v4
	v_mul_f32_e32 v41, v41, v161
	s_waitcnt vmcnt(4)
;     __device__ __forceinline__ void mid(f32x4 (&acc)[2][2][4][2], const pg8::Unit& u, int wr, int wc, int fr_, int fq) const {
;     ...
;                 for (int bj = 0; bj < 2; ++bj) { const size_t o = (size_t)(u.pm * 256 + ai * 128 + wr * 64 + m * 16 + fr) * INCP + u.pn * 256 + bj * 128 + wc * 32 + 8 * fq;
;                     const u32x4 ga = *(const u32x4*)(PROJ + o + C_GA), gb = *(const u32x4*)(PROJ + o + C_GB);
; #pragma unroll
;                     for (int i = 0; i < 4; ++i) { const float r0 = bflo(ga[i]) * __builtin_amdgcn_rcpf(bflo(gb[i])), r1 = bfhi(ga[i]) * __builtin_amdgcn_rcpf(bfhi(gb[i]));
;                         acc[ai][bj][m][i >> 1][2 * (i & 1)] *= r0; acc[ai][bj][m][i >> 1][2 * (i & 1) + 1] *= r1; }
;                     __builtin_amdgcn_sched_barrier(0); }
	v_lshlrev_b32_e32 v4, 16, v170
	v_and_b32_e32 v170, 0xffff0000, v170
	v_rcp_f32_e32 v4, v4
	v_rcp_f32_e32 v170, v170
	v_lshlrev_b32_e32 v5, 16, v166
	v_and_b32_e32 v166, 0xffff0000, v166
	v_mul_f32_e32 v4, v4, v5
	v_mul_f32_e32 v166, v170, v166
	v_mul_f32_e32 v34, v34, v4
	v_mul_f32_e32 v35, v35, v166
	v_lshlrev_b32_e32 v4, 16, v171
	v_and_b32_e32 v171, 0xffff0000, v171
	v_rcp_f32_e32 v4, v4
	v_rcp_f32_e32 v171, v171
	v_lshlrev_b32_e32 v5, 16, v167
	v_and_b32_e32 v167, 0xffff0000, v167
	v_mul_f32_e32 v4, v4, v5
	v_mul_f32_e32 v167, v171, v167
	v_mul_f32_e32 v36, v36, v4
	v_mul_f32_e32 v37, v37, v167
	v_lshlrev_b32_e32 v4, 16, v172
	v_and_b32_e32 v172, 0xffff0000, v172
	v_rcp_f32_e32 v4, v4
	v_rcp_f32_e32 v172, v172
	v_lshlrev_b32_e32 v5, 16, v168
	v_and_b32_e32 v168, 0xffff0000, v168
	v_mul_f32_e32 v4, v4, v5
	v_mul_f32_e32 v168, v172, v168
	v_mul_f32_e32 v30, v30, v4
	v_mul_f32_e32 v31, v31, v168
	v_lshlrev_b32_e32 v4, 16, v173
	v_and_b32_e32 v173, 0xffff0000, v173
	v_rcp_f32_e32 v4, v4
	v_rcp_f32_e32 v173, v173
	v_lshlrev_b32_e32 v5, 16, v169
	v_and_b32_e32 v169, 0xffff0000, v169
	v_mul_f32_e32 v4, v4, v5
	v_mul_f32_e32 v169, v173, v169
	v_mul_f32_e32 v32, v32, v4
	v_mul_f32_e32 v33, v33, v169
	v_lshlrev_b32_e32 v4, 16, v178
	v_and_b32_e32 v178, 0xffff0000, v178
	v_rcp_f32_e32 v4, v4
	v_rcp_f32_e32 v178, v178
	v_lshlrev_b32_e32 v5, 16, v174
	v_and_b32_e32 v174, 0xffff0000, v174
	v_mul_f32_e32 v4, v4, v5
	v_mul_f32_e32 v174, v178, v174
	v_mul_f32_e32 v26, v26, v4
	v_mul_f32_e32 v27, v27, v174
	v_lshlrev_b32_e32 v4, 16, v179
	v_and_b32_e32 v179, 0xffff0000, v179
	v_rcp_f32_e32 v4, v4
	v_rcp_f32_e32 v179, v179
	v_lshlrev_b32_e32 v5, 16, v175
	v_and_b32_e32 v175, 0xffff0000, v175
	v_mul_f32_e32 v4, v4, v5
	v_mul_f32_e32 v175, v179, v175
	v_mul_f32_e32 v28, v28, v4
	v_mul_f32_e32 v29, v29, v175
	v_lshlrev_b32_e32 v4, 16, v180
	v_and_b32_e32 v180, 0xffff0000, v180
	v_rcp_f32_e32 v4, v4
	v_rcp_f32_e32 v180, v180
	v_lshlrev_b32_e32 v5, 16, v176
	v_and_b32_e32 v176, 0xffff0000, v176
	v_mul_f32_e32 v4, v4, v5
	v_mul_f32_e32 v176, v180, v176
	v_mul_f32_e32 v22, v22, v4
	v_mul_f32_e32 v23, v23, v176
	v_lshlrev_b32_e32 v4, 16, v181
	v_and_b32_e32 v181, 0xffff0000, v181
	v_rcp_f32_e32 v4, v4
	v_rcp_f32_e32 v181, v181
	v_lshlrev_b32_e32 v5, 16, v177
	v_and_b32_e32 v177, 0xffff0000, v177
	v_mul_f32_e32 v4, v4, v5
	v_mul_f32_e32 v177, v181, v177
	v_mul_f32_e32 v24, v24, v4
	v_mul_f32_e32 v25, v25, v177
	s_waitcnt vmcnt(0)
	v_lshlrev_b32_e32 v4, 16, v186
	v_and_b32_e32 v186, 0xffff0000, v186
	v_rcp_f32_e32 v4, v4
	v_rcp_f32_e32 v186, v186
	v_lshlrev_b32_e32 v5, 16, v182
	v_and_b32_e32 v182, 0xffff0000, v182
	v_mul_f32_e32 v4, v4, v5
	v_mul_f32_e32 v182, v186, v182
	v_mul_f32_e32 v18, v18, v4
	v_mul_f32_e32 v19, v19, v182
	v_lshlrev_b32_e32 v4, 16, v187
	v_and_b32_e32 v187, 0xffff0000, v187
	v_rcp_f32_e32 v4, v4
	v_rcp_f32_e32 v187, v187
	v_lshlrev_b32_e32 v5, 16, v183
	v_and_b32_e32 v183, 0xffff0000, v183
	v_mul_f32_e32 v4, v4, v5
	v_mul_f32_e32 v183, v187, v183
	v_mul_f32_e32 v20, v20, v4
	v_mul_f32_e32 v21, v21, v183
	v_lshlrev_b32_e32 v4, 16, v188
	v_and_b32_e32 v188, 0xffff0000, v188
	v_rcp_f32_e32 v4, v4
	v_rcp_f32_e32 v188, v188
	v_lshlrev_b32_e32 v5, 16, v184
	v_and_b32_e32 v184, 0xffff0000, v184
	v_mul_f32_e32 v4, v4, v5
	v_mul_f32_e32 v184, v188, v184
	v_mul_f32_e32 v14, v14, v4
	v_mul_f32_e32 v15, v15, v184
	v_lshlrev_b32_e32 v4, 16, v189
	v_and_b32_e32 v189, 0xffff0000, v189
	v_rcp_f32_e32 v4, v4
	v_rcp_f32_e32 v189, v189
	v_lshlrev_b32_e32 v5, 16, v185
	v_and_b32_e32 v185, 0xffff0000, v185
	v_mul_f32_e32 v4, v4, v5
	v_mul_f32_e32 v185, v189, v185
	v_mul_f32_e32 v16, v16, v4
	v_mul_f32_e32 v17, v17, v185
	v_lshlrev_b32_e32 v4, 16, v194
	v_and_b32_e32 v194, 0xffff0000, v194
	v_rcp_f32_e32 v4, v4
	v_rcp_f32_e32 v194, v194
	v_lshlrev_b32_e32 v5, 16, v190
	v_and_b32_e32 v190, 0xffff0000, v190
	v_mul_f32_e32 v4, v4, v5
	v_mul_f32_e32 v190, v194, v190
	v_mul_f32_e32 v10, v10, v4
	v_mul_f32_e32 v11, v11, v190
	v_lshlrev_b32_e32 v4, 16, v195
	v_and_b32_e32 v195, 0xffff0000, v195
	v_rcp_f32_e32 v4, v4
	v_rcp_f32_e32 v195, v195
	v_lshlrev_b32_e32 v5, 16, v191
	v_and_b32_e32 v191, 0xffff0000, v191
	v_mul_f32_e32 v4, v4, v5
	v_mul_f32_e32 v191, v195, v191
	v_mul_f32_e32 v12, v12, v4
	v_mul_f32_e32 v13, v13, v191
	v_lshlrev_b32_e32 v4, 16, v196
	v_and_b32_e32 v196, 0xffff0000, v196
	v_rcp_f32_e32 v4, v4
	v_rcp_f32_e32 v196, v196
	v_lshlrev_b32_e32 v5, 16, v192
	v_and_b32_e32 v192, 0xffff0000, v192
	v_mul_f32_e32 v4, v4, v5
	v_mul_f32_e32 v192, v196, v192
	v_mul_f32_e32 v6, v6, v4
	v_mul_f32_e32 v7, v7, v192
	v_lshlrev_b32_e32 v4, 16, v197
	v_and_b32_e32 v197, 0xffff0000, v197
	v_rcp_f32_e32 v4, v4
	v_rcp_f32_e32 v197, v197
	v_lshlrev_b32_e32 v5, 16, v193
	v_and_b32_e32 v193, 0xffff0000, v193
	v_mul_f32_e32 v4, v4, v5
	v_mul_f32_e32 v193, v197, v193
	v_mul_f32_e32 v8, v8, v4
	v_mul_f32_e32 v9, v9, v193

; #define PG8_TILE_BEGIN(acc, wr, wc, fr, fq) \
;     _Pragma("unroll") for (int ai = 0; ai < 2; ++ai) _Pragma("unroll") for (int m = 0; m < 4; ++m) _Pragma("unroll") for (int bj = 0; bj < 2; ++bj) { \
;         const int trow = ai * 128 + wr * 64 + m * 16 + fr, tcol = bj * 128 + wc * 32 + 8 * fq; f32x4 v0 = acc[ai][bj][m][0], v1 = acc[ai][bj][m][1];
; __device__ __forceinline__ u32x4 pack8(f32x4 v0, f32x4 v1) { u32x4 w; w.x = cvt_pk_bf16(v0[0], v0[1]); w.y = cvt_pk_bf16(v0[2], v0[3]); w.z = cvt_pk_bf16(v1[0], v1[1]); w.w = cvt_pk_bf16(v1[2], v1[3]); return w; }
;     __device__ __forceinline__ void operator()(const f32x4 (&acc)[2][2][4][2], const pg8::Unit& u, int wr, int wc, int fr, int fq) const {
;         PG8_TILE_BEGIN(acc, wr, wc, fr, fq)
;             const int row = u.pm * 256 + trow, col = u.pn * 256 + tcol;
;             const u32x4 g = *(const u32x4*)(PROJ + (size_t)row * INCP + C_GB + col);
;             v0[0] *= bflo(g.x); v0[1] *= bfhi(g.x); v0[2] *= bflo(g.y); v0[3] *= bfhi(g.y); v1[0] *= bflo(g.z); v1[1] *= bfhi(g.z); v1[2] *= bflo(g.w); v1[3] *= bfhi(g.w);
;             *(u32x4*)(MRG + (size_t)row * DM + col) = pg8::pack8(v0, v1);
;         PG8_TILE_END
.LBB0_3608:
	v_readlane_b32 s4, v253, 54
	v_readlane_b32 s5, v253, 55
	v_add_u32_e32 v136, s17, v226
	v_or_b32_e32 v4, s20, v228
	v_mov_b64_e32 v[138:139], s[4:5]
	v_mad_i64_i32 v[134:135], s[4:5], v136, s48, v[138:139]
	v_ashrrev_i32_e32 v5, 31, v4
	v_lshl_add_u64 v[146:147], v[134:135], 0, s[14:15]
	v_lshlrev_b64 v[134:135], 1, v[4:5]
	v_lshl_add_u64 v[140:141], v[146:147], 0, v[134:135]
	global_load_dwordx4 v[140:143], v[140:141], off
	v_ashrrev_i32_e32 v137, 31, v136
	v_readlane_b32 s20, v254, 59
	v_lshlrev_b64 v[144:145], 11, v[136:137]
	v_readlane_b32 s21, v254, 60
	v_or_b32_e32 v4, 0x80, v4
	v_ashrrev_i32_e32 v5, 31, v4
	v_lshlrev_b64 v[4:5], 1, v[4:5]
	s_and_b64 vcc, exec, s[0:1]
	s_mov_b32 s59, s65
	v_lshl_add_u64 v[150:151], v[146:147], 0, v[4:5]
	global_load_dwordx4 v[150:153], v[150:151], off
	v_or_b32_e32 v148, 16, v136
	v_mad_i64_i32 v[148:149], s[4:5], v148, s48, v[138:139]
	v_lshl_add_u64 v[148:149], v[148:149], 0, s[14:15]
	v_lshl_add_u64 v[154:155], v[148:149], 0, v[134:135]
	global_load_dwordx4 v[154:157], v[154:155], off
	v_lshl_add_u64 v[158:159], v[148:149], 0, v[4:5]
	global_load_dwordx4 v[158:161], v[158:159], off
	v_or_b32_e32 v148, 32, v136
	v_mad_i64_i32 v[148:149], s[4:5], v148, s48, v[138:139]
	v_lshl_add_u64 v[148:149], v[148:149], 0, s[14:15]
	v_lshl_add_u64 v[162:163], v[148:149], 0, v[134:135]
	global_load_dwordx4 v[162:165], v[162:163], off
	v_lshl_add_u64 v[166:167], v[148:149], 0, v[4:5]
	global_load_dwordx4 v[166:169], v[166:167], off
	v_or_b32_e32 v148, 48, v136
	v_mad_i64_i32 v[148:149], s[4:5], v148, s48, v[138:139]
	v_lshl_add_u64 v[148:149], v[148:149], 0, s[14:15]
	v_lshl_add_u64 v[170:171], v[148:149], 0, v[134:135]
	global_load_dwordx4 v[170:173], v[170:171], off
	v_lshl_add_u64 v[174:175], v[148:149], 0, v[4:5]
	global_load_dwordx4 v[174:177], v[174:175], off
	v_mov_b32_e32 v148, v136
	v_ashrrev_i32_e32 v149, 31, v148
	v_lshlrev_b64 v[148:149], 11, v[148:149]
	v_lshl_add_u64 v[146:147], s[20:21], 0, v[148:149]
	v_lshl_add_u64 v[146:147], v[146:147], 0, v[134:135]
	s_waitcnt vmcnt(7)
	v_lshlrev_b32_e32 v186, 16, v140
	v_and_b32_e32 v140, 0xffff0000, v140
	v_mul_f32_e32 v130, v130, v186
	v_mul_f32_e32 v131, v131, v140
	v_lshlrev_b32_e32 v186, 16, v141
	v_and_b32_e32 v141, 0xffff0000, v141
	v_mul_f32_e32 v132, v132, v186
	v_mul_f32_e32 v133, v133, v141
	v_lshlrev_b32_e32 v186, 16, v142
	v_and_b32_e32 v142, 0xffff0000, v142
	v_mul_f32_e32 v182, v126, v186
	v_mul_f32_e32 v183, v127, v142
	v_lshlrev_b32_e32 v186, 16, v143
	v_and_b32_e32 v143, 0xffff0000, v143
	v_mul_f32_e32 v184, v128, v186
	v_mul_f32_e32 v185, v129, v143
	v_cvt_pk_bf16_f32 v126, v130, v131
	v_cvt_pk_bf16_f32 v127, v132, v133
	v_cvt_pk_bf16_f32 v128, v182, v183
	v_cvt_pk_bf16_f32 v129, v184, v185
	global_store_dwordx4 v[146:147], v[126:129], off
	s_waitcnt vmcnt(7)
	v_lshlrev_b32_e32 v186, 16, v150
	v_and_b32_e32 v150, 0xffff0000, v150
	v_mul_f32_e32 v122, v122, v186
	v_mul_f32_e32 v123, v123, v150
	v_lshlrev_b32_e32 v186, 16, v151
	v_and_b32_e32 v151, 0xffff0000, v151
	v_mul_f32_e32 v124, v124, v186
	v_mul_f32_e32 v125, v125, v151
	v_lshlrev_b32_e32 v186, 16, v152
	v_and_b32_e32 v152, 0xffff0000, v152
	v_mul_f32_e32 v182, v118, v186
	v_mul_f32_e32 v183, v119, v152
	v_lshlrev_b32_e32 v186, 16, v153
	v_and_b32_e32 v153, 0xffff0000, v153
	v_mul_f32_e32 v184, v120, v186
	v_mul_f32_e32 v185, v121, v153
	v_cvt_pk_bf16_f32 v118, v122, v123
	v_cvt_pk_bf16_f32 v119, v124, v125
	v_cvt_pk_bf16_f32 v120, v182, v183
	v_cvt_pk_bf16_f32 v121, v184, v185
	global_store_dwordx4 v[146:147], v[118:121], off offset:256
	v_or_b32_e32 v148, 16, v136
	v_ashrrev_i32_e32 v149, 31, v148
	v_lshlrev_b64 v[148:149], 11, v[148:149]
	v_lshl_add_u64 v[146:147], s[20:21], 0, v[148:149]
	v_lshl_add_u64 v[146:147], v[146:147], 0, v[134:135]
	s_waitcnt vmcnt(7)
	v_lshlrev_b32_e32 v186, 16, v154
	v_and_b32_e32 v154, 0xffff0000, v154
	v_mul_f32_e32 v114, v114, v186
	v_mul_f32_e32 v115, v115, v154
	v_lshlrev_b32_e32 v186, 16, v155
	v_and_b32_e32 v155, 0xffff0000, v155
	v_mul_f32_e32 v116, v116, v186
	v_mul_f32_e32 v117, v117, v155
	v_lshlrev_b32_e32 v186, 16, v156
	v_and_b32_e32 v156, 0xffff0000, v156
	v_mul_f32_e32 v182, v110, v186
	v_mul_f32_e32 v183, v111, v156
	v_lshlrev_b32_e32 v186, 16, v157
	v_and_b32_e32 v157, 0xffff0000, v157
	v_mul_f32_e32 v184, v112, v186
	v_mul_f32_e32 v185, v113, v157
	v_cvt_pk_bf16_f32 v110, v114, v115
	v_cvt_pk_bf16_f32 v111, v116, v117
	v_cvt_pk_bf16_f32 v112, v182, v183
	v_cvt_pk_bf16_f32 v113, v184, v185
	global_store_dwordx4 v[146:147], v[110:113], off
	s_waitcnt vmcnt(7)
	v_lshlrev_b32_e32 v186, 16, v158
	v_and_b32_e32 v158, 0xffff0000, v158
	v_mul_f32_e32 v106, v106, v186
	v_mul_f32_e32 v107, v107, v158
	v_lshlrev_b32_e32 v186, 16, v159
	v_and_b32_e32 v159, 0xffff0000, v159
	v_mul_f32_e32 v108, v108, v186
	v_mul_f32_e32 v109, v109, v159
	v_lshlrev_b32_e32 v186, 16, v160
	v_and_b32_e32 v160, 0xffff0000, v160
	v_mul_f32_e32 v182, v102, v186
	v_mul_f32_e32 v183, v103, v160
	v_lshlrev_b32_e32 v186, 16, v161
	v_and_b32_e32 v161, 0xffff0000, v161
	v_mul_f32_e32 v184, v104, v186
	v_mul_f32_e32 v185, v105, v161
	v_cvt_pk_bf16_f32 v102, v106, v107
	v_cvt_pk_bf16_f32 v103, v108, v109
	v_cvt_pk_bf16_f32 v104, v182, v183
	v_cvt_pk_bf16_f32 v105, v184, v185
	global_store_dwordx4 v[146:147], v[102:105], off offset:256
	v_or_b32_e32 v148, 32, v136
	v_ashrrev_i32_e32 v149, 31, v148
	v_lshlrev_b64 v[148:149], 11, v[148:149]
	v_lshl_add_u64 v[146:147], s[20:21], 0, v[148:149]
	v_lshl_add_u64 v[146:147], v[146:147], 0, v[134:135]
	s_waitcnt vmcnt(7)
; #define PG8_TILE_BEGIN(acc, wr, wc, fr, fq) \
;     _Pragma("unroll") for (int ai = 0; ai < 2; ++ai) _Pragma("unroll") for (int m = 0; m < 4; ++m) _Pragma("unroll") for (int bj = 0; bj < 2; ++bj) { \
;         const int trow = ai * 128 + wr * 64 + m * 16 + fr, tcol = bj * 128 + wc * 32 + 8 * fq; f32x4 v0 = acc[ai][bj][m][0], v1 = acc[ai][bj][m][1];
; __device__ __forceinline__ u32x4 pack8(f32x4 v0, f32x4 v1) { u32x4 w; w.x = cvt_pk_bf16(v0[0], v0[1]); w.y = cvt_pk_bf16(v0[2], v0[3]); w.z = cvt_pk_bf16(v1[0], v1[1]); w.w = cvt_pk_bf16(v1[2], v1[3]); return w; }
;     __device__ __forceinline__ void operator()(const f32x4 (&acc)[2][2][4][2], const pg8::Unit& u, int wr, int wc, int fr, int fq) const {
;         PG8_TILE_BEGIN(acc, wr, wc, fr, fq)
;             const int row = u.pm * 256 + trow, col = u.pn * 256 + tcol;
;             const u32x4 g = *(const u32x4*)(PROJ + (size_t)row * INCP + C_GB + col);
;             v0[0] *= bflo(g.x); v0[1] *= bfhi(g.x); v0[2] *= bflo(g.y); v0[3] *= bfhi(g.y); v1[0] *= bflo(g.z); v1[1] *= bfhi(g.z); v1[2] *= bflo(g.w); v1[3] *= bfhi(g.w);
;             *(u32x4*)(MRG + (size_t)row * DM + col) = pg8::pack8(v0, v1);
;         PG8_TILE_END
	v_lshlrev_b32_e32 v186, 16, v162
	v_and_b32_e32 v162, 0xffff0000, v162
	v_mul_f32_e32 v98, v98, v186
	v_mul_f32_e32 v99, v99, v162
	v_lshlrev_b32_e32 v186, 16, v163
	v_and_b32_e32 v163, 0xffff0000, v163
	v_mul_f32_e32 v100, v100, v186
	v_mul_f32_e32 v101, v101, v163
	v_lshlrev_b32_e32 v186, 16, v164
	v_and_b32_e32 v164, 0xffff0000, v164
	v_mul_f32_e32 v182, v94, v186
	v_mul_f32_e32 v183, v95, v164
	v_lshlrev_b32_e32 v186, 16, v165
	v_and_b32_e32 v165, 0xffff0000, v165
	v_mul_f32_e32 v184, v96, v186
	v_mul_f32_e32 v185, v97, v165
	v_cvt_pk_bf16_f32 v94, v98, v99
	v_cvt_pk_bf16_f32 v95, v100, v101
	v_cvt_pk_bf16_f32 v96, v182, v183
	v_cvt_pk_bf16_f32 v97, v184, v185
	global_store_dwordx4 v[146:147], v[94:97], off
	s_waitcnt vmcnt(7)
	v_lshlrev_b32_e32 v186, 16, v166
	v_and_b32_e32 v166, 0xffff0000, v166
	v_mul_f32_e32 v90, v90, v186
	v_mul_f32_e32 v91, v91, v166
	v_lshlrev_b32_e32 v186, 16, v167
	v_and_b32_e32 v167, 0xffff0000, v167
	v_mul_f32_e32 v92, v92, v186
	v_mul_f32_e32 v93, v93, v167
	v_lshlrev_b32_e32 v186, 16, v168
	v_and_b32_e32 v168, 0xffff0000, v168
	v_mul_f32_e32 v182, v86, v186
	v_mul_f32_e32 v183, v87, v168
	v_lshlrev_b32_e32 v186, 16, v169
	v_and_b32_e32 v169, 0xffff0000, v169
	v_mul_f32_e32 v184, v88, v186
	v_mul_f32_e32 v185, v89, v169
	v_cvt_pk_bf16_f32 v86, v90, v91
	v_cvt_pk_bf16_f32 v87, v92, v93
	v_cvt_pk_bf16_f32 v88, v182, v183
	v_cvt_pk_bf16_f32 v89, v184, v185
	global_store_dwordx4 v[146:147], v[86:89], off offset:256
	v_or_b32_e32 v148, 48, v136
	v_ashrrev_i32_e32 v149, 31, v148
	v_lshlrev_b64 v[148:149], 11, v[148:149]
	v_lshl_add_u64 v[146:147], s[20:21], 0, v[148:149]
	v_lshl_add_u64 v[146:147], v[146:147], 0, v[134:135]
	s_waitcnt vmcnt(7)
	v_lshlrev_b32_e32 v186, 16, v170
	v_and_b32_e32 v170, 0xffff0000, v170
	v_mul_f32_e32 v82, v82, v186
	v_mul_f32_e32 v83, v83, v170
	v_lshlrev_b32_e32 v186, 16, v171
	v_and_b32_e32 v171, 0xffff0000, v171
	v_mul_f32_e32 v84, v84, v186
	v_mul_f32_e32 v85, v85, v171
	v_lshlrev_b32_e32 v186, 16, v172
	v_and_b32_e32 v172, 0xffff0000, v172
	v_mul_f32_e32 v182, v78, v186
	v_mul_f32_e32 v183, v79, v172
	v_lshlrev_b32_e32 v186, 16, v173
	v_and_b32_e32 v173, 0xffff0000, v173
	v_mul_f32_e32 v184, v80, v186
	v_mul_f32_e32 v185, v81, v173
	v_cvt_pk_bf16_f32 v78, v82, v83
	v_cvt_pk_bf16_f32 v79, v84, v85
	v_cvt_pk_bf16_f32 v80, v182, v183
	v_cvt_pk_bf16_f32 v81, v184, v185
	global_store_dwordx4 v[146:147], v[78:81], off
	s_waitcnt vmcnt(7)
	v_lshlrev_b32_e32 v186, 16, v174
	v_and_b32_e32 v174, 0xffff0000, v174
	v_mul_f32_e32 v74, v74, v186
	v_mul_f32_e32 v75, v75, v174
	v_lshlrev_b32_e32 v186, 16, v175
	v_and_b32_e32 v175, 0xffff0000, v175
	v_mul_f32_e32 v76, v76, v186
	v_mul_f32_e32 v77, v77, v175
	v_lshlrev_b32_e32 v186, 16, v176
	v_and_b32_e32 v176, 0xffff0000, v176
	v_mul_f32_e32 v182, v70, v186
	v_mul_f32_e32 v183, v71, v176
	v_lshlrev_b32_e32 v186, 16, v177
	v_and_b32_e32 v177, 0xffff0000, v177
	v_mul_f32_e32 v184, v72, v186
	v_mul_f32_e32 v185, v73, v177
	v_cvt_pk_bf16_f32 v70, v74, v75
	v_cvt_pk_bf16_f32 v71, v76, v77
	v_cvt_pk_bf16_f32 v72, v182, v183
	v_cvt_pk_bf16_f32 v73, v184, v185
	global_store_dwordx4 v[146:147], v[70:73], off offset:256
	v_or_b32_e32 v148, 128, v136
	v_mad_i64_i32 v[148:149], s[4:5], v148, s48, v[138:139]
	v_lshl_add_u64 v[148:149], v[148:149], 0, s[14:15]
	v_lshl_add_u64 v[150:151], v[148:149], 0, v[134:135]
	global_load_dwordx4 v[150:153], v[150:151], off
	v_lshl_add_u64 v[154:155], v[148:149], 0, v[4:5]
	global_load_dwordx4 v[154:157], v[154:155], off
	v_or_b32_e32 v148, 144, v136
	v_mad_i64_i32 v[148:149], s[4:5], v148, s48, v[138:139]
	v_lshl_add_u64 v[148:149], v[148:149], 0, s[14:15]
	v_lshl_add_u64 v[158:159], v[148:149], 0, v[134:135]
	global_load_dwordx4 v[158:161], v[158:159], off
	v_lshl_add_u64 v[162:163], v[148:149], 0, v[4:5]
	global_load_dwordx4 v[162:165], v[162:163], off
	v_or_b32_e32 v148, 160, v136
	v_mad_i64_i32 v[148:149], s[4:5], v148, s48, v[138:139]
	v_lshl_add_u64 v[148:149], v[148:149], 0, s[14:15]
	v_lshl_add_u64 v[166:167], v[148:149], 0, v[134:135]
	global_load_dwordx4 v[166:169], v[166:167], off
	v_lshl_add_u64 v[170:171], v[148:149], 0, v[4:5]
	global_load_dwordx4 v[170:173], v[170:171], off
	v_or_b32_e32 v148, 176, v136
	v_mad_i64_i32 v[148:149], s[4:5], v148, s48, v[138:139]
	v_lshl_add_u64 v[148:149], v[148:149], 0, s[14:15]
	v_lshl_add_u64 v[174:175], v[148:149], 0, v[134:135]
	global_load_dwordx4 v[174:177], v[174:175], off
	v_lshl_add_u64 v[178:179], v[148:149], 0, v[4:5]
	global_load_dwordx4 v[178:181], v[178:179], off
	v_or_b32_e32 v148, 128, v136
	v_ashrrev_i32_e32 v149, 31, v148
	v_lshlrev_b64 v[148:149], 11, v[148:149]
	v_lshl_add_u64 v[146:147], s[20:21], 0, v[148:149]
	v_lshl_add_u64 v[146:147], v[146:147], 0, v[134:135]
	s_waitcnt vmcnt(7)
	v_lshlrev_b32_e32 v186, 16, v150
	v_and_b32_e32 v150, 0xffff0000, v150
	v_mul_f32_e32 v66, v66, v186
	v_mul_f32_e32 v67, v67, v150
	v_lshlrev_b32_e32 v186, 16, v151
	v_and_b32_e32 v151, 0xffff0000, v151
	v_mul_f32_e32 v68, v68, v186
	v_mul_f32_e32 v69, v69, v151
	v_lshlrev_b32_e32 v186, 16, v152
	v_and_b32_e32 v152, 0xffff0000, v152
	v_mul_f32_e32 v182, v62, v186
	v_mul_f32_e32 v183, v63, v152
	v_lshlrev_b32_e32 v186, 16, v153
	v_and_b32_e32 v153, 0xffff0000, v153
	v_mul_f32_e32 v184, v64, v186
	v_mul_f32_e32 v185, v65, v153
	v_cvt_pk_bf16_f32 v62, v66, v67
	v_cvt_pk_bf16_f32 v63, v68, v69
	v_cvt_pk_bf16_f32 v64, v182, v183
	v_cvt_pk_bf16_f32 v65, v184, v185
	global_store_dwordx4 v[146:147], v[62:65], off
	s_waitcnt vmcnt(7)
; #define PG8_TILE_BEGIN(acc, wr, wc, fr, fq) \
;     _Pragma("unroll") for (int ai = 0; ai < 2; ++ai) _Pragma("unroll") for (int m = 0; m < 4; ++m) _Pragma("unroll") for (int bj = 0; bj < 2; ++bj) { \
;         const int trow = ai * 128 + wr * 64 + m * 16 + fr, tcol = bj * 128 + wc * 32 + 8 * fq; f32x4 v0 = acc[ai][bj][m][0], v1 = acc[ai][bj][m][1];
; __device__ __forceinline__ u32x4 pack8(f32x4 v0, f32x4 v1) { u32x4 w; w.x = cvt_pk_bf16(v0[0], v0[1]); w.y = cvt_pk_bf16(v0[2], v0[3]); w.z = cvt_pk_bf16(v1[0], v1[1]); w.w = cvt_pk_bf16(v1[2], v1[3]); return w; }
;     __device__ __forceinline__ void operator()(const f32x4 (&acc)[2][2][4][2], const pg8::Unit& u, int wr, int wc, int fr, int fq) const {
;         PG8_TILE_BEGIN(acc, wr, wc, fr, fq)
;             const int row = u.pm * 256 + trow, col = u.pn * 256 + tcol;
;             const u32x4 g = *(const u32x4*)(PROJ + (size_t)row * INCP + C_GB + col);
;             v0[0] *= bflo(g.x); v0[1] *= bfhi(g.x); v0[2] *= bflo(g.y); v0[3] *= bfhi(g.y); v1[0] *= bflo(g.z); v1[1] *= bfhi(g.z); v1[2] *= bflo(g.w); v1[3] *= bfhi(g.w);
;             *(u32x4*)(MRG + (size_t)row * DM + col) = pg8::pack8(v0, v1);
;         PG8_TILE_END
	v_lshlrev_b32_e32 v186, 16, v154
	v_and_b32_e32 v154, 0xffff0000, v154
	v_mul_f32_e32 v58, v58, v186
	v_mul_f32_e32 v59, v59, v154
	v_lshlrev_b32_e32 v186, 16, v155
	v_and_b32_e32 v155, 0xffff0000, v155
	v_mul_f32_e32 v60, v60, v186
	v_mul_f32_e32 v61, v61, v155
	v_lshlrev_b32_e32 v186, 16, v156
	v_and_b32_e32 v156, 0xffff0000, v156
	v_mul_f32_e32 v182, v54, v186
	v_mul_f32_e32 v183, v55, v156
	v_lshlrev_b32_e32 v186, 16, v157
	v_and_b32_e32 v157, 0xffff0000, v157
	v_mul_f32_e32 v184, v56, v186
	v_mul_f32_e32 v185, v57, v157
	v_cvt_pk_bf16_f32 v54, v58, v59
	v_cvt_pk_bf16_f32 v55, v60, v61
	v_cvt_pk_bf16_f32 v56, v182, v183
	v_cvt_pk_bf16_f32 v57, v184, v185
	global_store_dwordx4 v[146:147], v[54:57], off offset:256
	v_or_b32_e32 v148, 144, v136
	v_ashrrev_i32_e32 v149, 31, v148
	v_lshlrev_b64 v[148:149], 11, v[148:149]
	v_lshl_add_u64 v[146:147], s[20:21], 0, v[148:149]
	v_lshl_add_u64 v[146:147], v[146:147], 0, v[134:135]
	s_waitcnt vmcnt(7)
	v_lshlrev_b32_e32 v186, 16, v158
	v_and_b32_e32 v158, 0xffff0000, v158
	v_mul_f32_e32 v50, v50, v186
	v_mul_f32_e32 v51, v51, v158
	v_lshlrev_b32_e32 v186, 16, v159
	v_and_b32_e32 v159, 0xffff0000, v159
	v_mul_f32_e32 v52, v52, v186
	v_mul_f32_e32 v53, v53, v159
	v_lshlrev_b32_e32 v186, 16, v160
	v_and_b32_e32 v160, 0xffff0000, v160
	v_mul_f32_e32 v182, v46, v186
	v_mul_f32_e32 v183, v47, v160
	v_lshlrev_b32_e32 v186, 16, v161
	v_and_b32_e32 v161, 0xffff0000, v161
	v_mul_f32_e32 v184, v48, v186
	v_mul_f32_e32 v185, v49, v161
	v_cvt_pk_bf16_f32 v46, v50, v51
	v_cvt_pk_bf16_f32 v47, v52, v53
	v_cvt_pk_bf16_f32 v48, v182, v183
	v_cvt_pk_bf16_f32 v49, v184, v185
	global_store_dwordx4 v[146:147], v[46:49], off
	s_waitcnt vmcnt(7)
	v_lshlrev_b32_e32 v186, 16, v162
	v_and_b32_e32 v162, 0xffff0000, v162
	v_mul_f32_e32 v42, v42, v186
	v_mul_f32_e32 v43, v43, v162
	v_lshlrev_b32_e32 v186, 16, v163
	v_and_b32_e32 v163, 0xffff0000, v163
	v_mul_f32_e32 v44, v44, v186
	v_mul_f32_e32 v45, v45, v163
	v_lshlrev_b32_e32 v186, 16, v164
	v_and_b32_e32 v164, 0xffff0000, v164
	v_mul_f32_e32 v182, v38, v186
	v_mul_f32_e32 v183, v39, v164
	v_lshlrev_b32_e32 v186, 16, v165
	v_and_b32_e32 v165, 0xffff0000, v165
	v_mul_f32_e32 v184, v40, v186
	v_mul_f32_e32 v185, v41, v165
	v_cvt_pk_bf16_f32 v38, v42, v43
	v_cvt_pk_bf16_f32 v39, v44, v45
	v_cvt_pk_bf16_f32 v40, v182, v183
	v_cvt_pk_bf16_f32 v41, v184, v185
	global_store_dwordx4 v[146:147], v[38:41], off offset:256
	v_or_b32_e32 v148, 160, v136
	v_ashrrev_i32_e32 v149, 31, v148
	v_lshlrev_b64 v[148:149], 11, v[148:149]
	v_lshl_add_u64 v[146:147], s[20:21], 0, v[148:149]
	v_lshl_add_u64 v[146:147], v[146:147], 0, v[134:135]
	s_waitcnt vmcnt(7)
	v_lshlrev_b32_e32 v186, 16, v166
	v_and_b32_e32 v166, 0xffff0000, v166
	v_mul_f32_e32 v34, v34, v186
	v_mul_f32_e32 v35, v35, v166
	v_lshlrev_b32_e32 v186, 16, v167
	v_and_b32_e32 v167, 0xffff0000, v167
	v_mul_f32_e32 v36, v36, v186
	v_mul_f32_e32 v37, v37, v167
	v_lshlrev_b32_e32 v186, 16, v168
	v_and_b32_e32 v168, 0xffff0000, v168
	v_mul_f32_e32 v182, v30, v186
	v_mul_f32_e32 v183, v31, v168
	v_lshlrev_b32_e32 v186, 16, v169
	v_and_b32_e32 v169, 0xffff0000, v169
	v_mul_f32_e32 v184, v32, v186
	v_mul_f32_e32 v185, v33, v169
	v_cvt_pk_bf16_f32 v30, v34, v35
	v_cvt_pk_bf16_f32 v31, v36, v37
	v_cvt_pk_bf16_f32 v32, v182, v183
	v_cvt_pk_bf16_f32 v33, v184, v185
	global_store_dwordx4 v[146:147], v[30:33], off
	s_waitcnt vmcnt(7)
	v_lshlrev_b32_e32 v186, 16, v170
	v_and_b32_e32 v170, 0xffff0000, v170
	v_mul_f32_e32 v26, v26, v186
	v_mul_f32_e32 v27, v27, v170
	v_lshlrev_b32_e32 v186, 16, v171
	v_and_b32_e32 v171, 0xffff0000, v171
	v_mul_f32_e32 v28, v28, v186
	v_mul_f32_e32 v29, v29, v171
	v_lshlrev_b32_e32 v186, 16, v172
	v_and_b32_e32 v172, 0xffff0000, v172
	v_mul_f32_e32 v182, v22, v186
	v_mul_f32_e32 v183, v23, v172
	v_lshlrev_b32_e32 v186, 16, v173
	v_and_b32_e32 v173, 0xffff0000, v173
	v_mul_f32_e32 v184, v24, v186
	v_mul_f32_e32 v185, v25, v173
	v_cvt_pk_bf16_f32 v22, v26, v27
	v_cvt_pk_bf16_f32 v23, v28, v29
	v_cvt_pk_bf16_f32 v24, v182, v183
	v_cvt_pk_bf16_f32 v25, v184, v185
	global_store_dwordx4 v[146:147], v[22:25], off offset:256
	v_or_b32_e32 v148, 176, v136
	v_ashrrev_i32_e32 v149, 31, v148
	v_lshlrev_b64 v[148:149], 11, v[148:149]
	v_lshl_add_u64 v[146:147], s[20:21], 0, v[148:149]
	v_lshl_add_u64 v[146:147], v[146:147], 0, v[134:135]
	s_waitcnt vmcnt(7)
	v_lshlrev_b32_e32 v186, 16, v174
	v_and_b32_e32 v174, 0xffff0000, v174
	v_mul_f32_e32 v18, v18, v186
	v_mul_f32_e32 v19, v19, v174
	v_lshlrev_b32_e32 v186, 16, v175
	v_and_b32_e32 v175, 0xffff0000, v175
	v_mul_f32_e32 v20, v20, v186
	v_mul_f32_e32 v21, v21, v175
	v_lshlrev_b32_e32 v186, 16, v176
	v_and_b32_e32 v176, 0xffff0000, v176
	v_mul_f32_e32 v182, v14, v186
	v_mul_f32_e32 v183, v15, v176
	v_lshlrev_b32_e32 v186, 16, v177
	v_and_b32_e32 v177, 0xffff0000, v177
	v_mul_f32_e32 v184, v16, v186
	v_mul_f32_e32 v185, v17, v177
	v_cvt_pk_bf16_f32 v14, v18, v19
	v_cvt_pk_bf16_f32 v15, v20, v21
	v_cvt_pk_bf16_f32 v16, v182, v183
	v_cvt_pk_bf16_f32 v17, v184, v185
	global_store_dwordx4 v[146:147], v[14:17], off
	s_waitcnt vmcnt(7)
	v_lshlrev_b32_e32 v186, 16, v178
	v_and_b32_e32 v178, 0xffff0000, v178
	v_mul_f32_e32 v10, v10, v186
	v_mul_f32_e32 v11, v11, v178
	v_lshlrev_b32_e32 v186, 16, v179
	v_and_b32_e32 v179, 0xffff0000, v179
	v_mul_f32_e32 v12, v12, v186
	v_mul_f32_e32 v13, v13, v179
	v_lshlrev_b32_e32 v186, 16, v180
	v_and_b32_e32 v180, 0xffff0000, v180
	v_mul_f32_e32 v182, v6, v186
	v_mul_f32_e32 v183, v7, v180
	v_lshlrev_b32_e32 v186, 16, v181
	v_and_b32_e32 v181, 0xffff0000, v181
	v_mul_f32_e32 v184, v8, v186
	v_mul_f32_e32 v185, v9, v181
	v_cvt_pk_bf16_f32 v6, v10, v11
	v_cvt_pk_bf16_f32 v7, v12, v13
	v_cvt_pk_bf16_f32 v8, v182, v183
	v_cvt_pk_bf16_f32 v9, v184, v185
	global_store_dwordx4 v[146:147], v[6:9], off offset:256
	s_mov_b64 s[4:5], -1
	s_cbranch_vccnz .LBB0_3587
	s_andn2_b64 vcc, exec, s[10:11]
	s_cbranch_vccnz .LBB0_3586
	s_barrier
	s_branch .LBB0_3586
